# scan: per-step keep-select replaced by DPP bank-masked write, y flushed every 4 steps
# speedup vs baseline: 1.0209x; 1.0168x over previous
; #define LAS __attribute__((address_space(3)))
; __device__ __forceinline__ void p4_scan(Frame& F) {
;     ...
;     for (int task = F.bx; task < NB * NH * 2 * 2; task += F.G) {
;         const int hf = (task >> 3) & 1, id_ = ((task >> 4) << 3) | (task & 7), d = id_ & 1, h = (id_ >> 1) & 15, b = id_ >> 5;
;         __syncthreads();
;         if (F.wave >= 4) {
;             const int lt = F.tid - 256, lstep = lt >> 3, lpc = lt & 7;
;             const bf16_t* Up = WSP(bf16_t, WS_SC) + (size_t)d * (SC_STRIDE / 2); const bf16_t* SBb = WSP(bf16_t, WS_SB);
;             const bf16_t* arr[4] = { SBb + (size_t)SB_NKK * (SB_STRIDE / 2), SBb + (size_t)(SB_BB + d) * (SB_STRIDE / 2), SBb + (size_t)(SB_KD + d) * (SB_STRIDE / 2), SBb + (size_t)SB_R * (SB_STRIDE / 2) };
;             const bf16_t* Vp = SBb + (size_t)SB_V * (SB_STRIDE / 2);
;             struct Stage { u32x4 w; u32x4 o[4]; u32x4 v; };
;             Stage sy;
;     ...
;             P4_ISSUE(sy, 0); P4_COMMIT(sy, 0);
;             P4_ISSUE(sy, 1);
;             LAS unsigned char* cvtile = F.lds + YB_OFF + 2 * YB_BYTES;
;             const int cvkq = F.wave - 4; int cvcur = 0, cvpb = 0; bool cvpend = false; unsigned char* cvpdst = nullptr;
;             const int cvstride = F.G * 4; int cvit = (task == F.bx) ? F.bx * 4 + (F.wave - 4) : CV_ITEMS;
;             f32x4 cvv[16]; CvItem cvt = cv_decode(F, cvit < CV_ITEMS ? cvit : 0); bool cvhave = cvit < CV_ITEMS;
;             if (cvhave) CV_LOAD(cvv, cvt, F.lane);
;             const int cvph = (F.bx >> 3) % 17;
;     ...
;             const int g = F.lane >> 4, kap = F.lane & 15, rown = 8 * F.wave + 2 * g + (kap & 1), roth = rown ^ 1;
;             f32x2 s0 = {0.f, 0.f}, s1 = {0.f, 0.f}, s2 = {0.f, 0.f}, s3 = {0.f, 0.f};
;             asm volatile("s_waitcnt lgkmcnt(0)" ::: "memory"); __builtin_amdgcn_s_barrier(); asm volatile("" ::: "memory");
;             for (int blk = 0; blk < NBLK; ++blk) {
;                 const LAS unsigned char* sb = F.lds + (blk & 1) * SLOT_BYTES;
;                 LAS float* yb = (LAS float*)(F.lds + YB_OFF + (blk & 1) * YB_BYTES);
;                 const unsigned aK = (unsigned)(size_t)(sb) + kap * 16, aVo = (unsigned)(size_t)(sb) + 5 * (SB * 256) + rown * 4, aVt = (unsigned)(size_t)(sb) + 5 * (SB * 256) + roth * 4;
.LBB0_482:
	s_cmp_lt_i32 s20, 5
	s_cselect_b64 s[0:1], -1, 0
	s_cmp_gt_i32 s21, 4
	s_cselect_b64 s[2:3], -1, 0
	s_and_b64 s[0:1], s[0:1], s[2:3]
	s_andn2_b64 vcc, exec, s[0:1]
	v_writelane_b32 v254, s79, 38
	s_cbranch_vccnz .LBB0_645
	s_cmpk_lt_i32 s91, 0x100
	s_cselect_b64 s[0:1], -1, 0
	s_cmpk_gt_i32 s91, 0xff
	s_movk_i32 s71, 0x100
	s_cbranch_scc1 .LBB0_566
	s_add_u32 s74, s96, 0x6ec00000
	s_addc_u32 s75, s97, 0
	v_readlane_b32 s2, v254, 33
	s_cmpk_lt_u32 s2, 0x100
	v_readlane_b32 s23, v254, 35
	v_lshrrev_b32_e32 v3, 3, v0
	s_cselect_b64 s[30:31], -1, 0
	s_lshl_b32 s2, s23, 3
	v_and_b32_e32 v3, 6, v3
	v_and_b32_e32 v4, 1, v0
	s_add_i32 s22, 0, 0x16000
	v_and_b32_e32 v2, 15, v0
	v_or3_b32 v3, v3, s2, v4
	v_and_b32_e32 v4, 7, v0
	s_add_u32 s76, s96, 0x44800000
	v_lshlrev_b32_e32 v91, 4, v2
	v_lshlrev_b32_e32 v99, 2, v3
	v_bfe_u32 v3, v0, 1, 3
	v_cmp_gt_u32_e64 s[4:5], 2, v2
	v_add_u32_e32 v2, 0xffffff00, v0
	s_addc_u32 s77, s97, 0
	v_mov_b32_e32 v93, 0
	v_lshlrev_b32_e32 v92, 4, v4
	v_cmp_eq_u32_e64 s[6:7], 1, v3
	v_cmp_eq_u32_e64 s[8:9], 2, v3
	v_cmp_eq_u32_e64 s[10:11], 3, v3
	v_cmp_eq_u32_e64 s[12:13], 4, v3
	v_cmp_eq_u32_e64 s[14:15], 5, v3
	v_cmp_eq_u32_e64 s[16:17], 6, v3
	v_cmp_eq_u32_e64 s[18:19], 7, v3
	v_lshlrev_b32_e32 v6, 7, v3
	v_ashrrev_i32_e32 v128, 3, v2
	s_add_u32 s78, s96, 0x4d000000
	v_lshl_add_u64 v[2:3], s[96:97], 0, v[92:93]
	s_mov_b64 s[2:3], 0x55800000
	s_addc_u32 s79, s97, 0
	v_lshl_add_u64 v[94:95], v[2:3], 0, s[2:3]
	s_mov_b64 s[2:3], 0x59c00000
	s_add_u32 s36, s96, 0x57a00000
	v_lshl_add_u64 v[96:97], v[2:3], 0, s[2:3]
	v_readlane_b32 s3, v254, 38
	s_addc_u32 s37, s97, 0
	s_lshl_b32 s80, s3, 2
	s_ashr_i32 s3, s91, 3
	s_add_i32 s2, s23, -4
	s_mul_hi_i32 s23, s3, 0x78787879
	s_lshr_b32 s24, s23, 31
	s_ashr_i32 s23, s23, 3
	s_add_i32 s23, s23, s24
	s_mul_i32 s23, s23, 17
	s_sub_i32 s3, s3, s23
	s_mul_i32 s3, s3, 12
	v_lshlrev_b32_e32 v132, 7, v128
	s_add_i32 s24, 0, 0x15000
	s_add_i32 s82, s3, 12
	v_add_u32_e32 v8, s24, v132
	s_sext_i32_i16 s24, s82
	s_mulk_i32 s24, 0x7879
	s_lshr_b32 s25, s24, 31
	s_ashr_i32 s24, s24, 19
	s_add_i32 s24, s24, s25
	s_sext_i32_i16 s25, s3
	s_mulk_i32 s25, 0x7879
	v_lshrrev_b32_e32 v3, 1, v0
	s_lshr_b32 s26, s25, 31
	s_ashr_i32 s25, s25, 19
	v_lshlrev_b32_e32 v130, 8, v128
	s_lshl_b32 s81, s91, 2
	v_and_b32_e32 v135, 16, v3
	v_lshlrev_b32_e32 v3, 2, v0
	s_add_i32 s25, s25, s26
	v_add_u32_e32 v2, 0, v130
	v_lshlrev_b32_e32 v131, 5, v4
	s_add_i32 s81, s81, s2
	v_and_b32_e32 v98, 0x7c, v3
	s_lshl_b32 s23, s2, 1
	s_and_b32 s25, s25, 0xffff
	s_and_b32 s24, s24, 0xffff
	v_lshrrev_b32_e32 v3, 5, v1
	v_lshlrev_b32_e32 v90, 3, v4
	v_cmp_gt_u32_e64 s[20:21], 4, v4
	v_sub_u32_e32 v7, v2, v132
	v_lshlrev_b32_e32 v102, 2, v4
	v_add_u32_e32 v137, v2, v131
	s_cmp_lg_u32 s24, s25
	v_lshlrev_b32_e32 v2, 9, v0
	v_bitop3_b32 v4, v3, v4, s23 bitop3:0x36
	s_cselect_b64 s[42:43], -1, 0
	v_and_b32_e32 v2, 0x3e00, v2
	s_add_i32 s24, 0, 0x18000
	v_lshlrev_b32_e32 v4, 4, v4
	v_add3_u32 v140, s24, v2, v4
	v_lshrrev_b32_e32 v2, 3, v1
	v_xor_b32_e32 v3, v3, v0
	v_lshl_or_b32 v2, s2, 5, v2
	v_lshlrev_b32_e32 v4, 4, v0
	v_lshlrev_b32_e32 v3, 4, v3
	v_and_b32_e32 v104, 0x70, v4
	v_and_b32_e32 v143, 0x70, v3
	v_mov_b32_e32 v3, v93
	v_or_b32_e32 v4, 8, v2
	v_lshlrev_b64 v[106:107], 11, v[2:3]
	v_lshrrev_b32_e32 v3, 2, v4
	v_xor_b32_e32 v3, v3, v0
	v_mov_b32_e32 v5, v93
	s_add_i32 s2, s3, 0x654
	s_add_i32 s23, s3, 0x660
	v_lshlrev_b32_e32 v144, 7, v4
	v_lshlrev_b32_e32 v3, 4, v3
	v_lshlrev_b64 v[108:109], 11, v[4:5]
	v_or_b32_e32 v4, 16, v2
	s_mul_hi_u32 s23, s23, 0xf0f0f0f1
	s_mul_hi_u32 s24, s2, 0xf0f0f0f1
	v_and_b32_e32 v145, 0x70, v3
	v_lshrrev_b32_e32 v3, 2, v4
	s_lshr_b32 s23, s23, 4
	s_lshr_b32 s24, s24, 4
	v_xor_b32_e32 v3, v3, v0
	s_cmp_lg_u32 s23, s24
	v_lshlrev_b32_e32 v142, 7, v2
	v_lshlrev_b32_e32 v3, 4, v3
	v_or_b32_e32 v2, 24, v2
	s_cselect_b64 s[44:45], -1, 0
	s_addk_i32 s3, 0x648
	s_mul_hi_i32 s2, s2, 0x78787879
	v_add3_u32 v141, s22, v132, v92
	v_and_b32_e32 v147, 0x70, v3
	v_lshrrev_b32_e32 v3, 2, v2
	v_add3_u32 v155, s22, v6, v99
	v_bfe_u32 v196, v0, 2, 2
	v_lshlrev_b32_e32 v196, 7, v196
	v_add3_u32 v196, s22, v196, v99
	s_lshr_b32 s22, s2, 31
	s_ashr_i32 s2, s2, 3
	s_mul_hi_i32 s3, s3, 0x78787879
	v_xor_b32_e32 v3, v3, v0
	s_add_i32 s2, s2, s22
	s_lshr_b32 s22, s3, 31
	s_ashr_i32 s3, s3, 3
	v_lshlrev_b32_e32 v3, 4, v3
	s_add_i32 s23, 0, 0x17000
	s_add_i32 s3, s3, s22
	v_and_b32_e32 v149, 0x70, v3
	v_mov_b32_e32 v3, v93
	s_cmp_lg_u32 s2, s3
	v_xor_b32_e32 v103, 4, v99
	s_mov_b32 s35, 0
	v_sub_u32_e32 v129, 0xff, v128
	v_add_u32_e32 v133, 32, v128
	v_sub_u32_e32 v134, 0xdf, v128
	v_add_u32_e32 v136, 64, v128
	v_lshl_add_u64 v[100:101], s[36:37], 0, v[92:93]
	v_add_u32_e32 v138, 0xb000, v137
	v_sub_u32_e32 v139, 0xbf, v128
	v_mov_b32_e32 v105, v93
	v_lshlrev_b32_e32 v146, 7, v4
	v_lshlrev_b64 v[110:111], 11, v[4:5]
	v_lshlrev_b32_e32 v148, 7, v2
	v_lshlrev_b64 v[112:113], 11, v[2:3]
	v_add_u32_e32 v150, 0xfc0, v128
	v_sub_u32_e32 v151, 63, v128
	v_add_u32_e32 v152, 0xfe0, v128
	v_sub_u32_e32 v153, 31, v128
	v_add3_u32 v154, s23, v132, v92
	s_cselect_b64 s[54:55], -1, 0
	v_sub_u32_e32 v156, 0, v128
	v_add_u32_e32 v157, v7, v131
	v_add_u32_e32 v158, v8, v131
	v_mov_b32_e32 v159, 0x10ff
	v_mov_b32_e32 v160, 0xff
	s_mov_b32 s83, s91
	s_branch .LBB0_487

; #define LAS __attribute__((address_space(3)))
; #define P4_RDSET(P, base_, boff_, vo_, vt_, voff_) do { P##w = lds_rd128<(boff_)>(base_); P##a = lds_rd128<(boff_) + SB * 256>(base_); P##b = lds_rd128<(boff_) + 2 * SB * 256>(base_); \
;                     P##k = lds_rd128<(boff_) + 3 * SB * 256>(base_); P##r = lds_rd128<(boff_) + 4 * SB * 256>(base_); P##vo = lds_rd32<(voff_)>(vo_); P##vt = lds_rd32<(voff_)>(vt_); } while (0)
; __device__ __forceinline__ void p4_scan(Frame& F) {
;     ...
;                 const LAS unsigned char* sb = F.lds + (blk & 1) * SLOT_BYTES;
;                 LAS float* yb = (LAS float*)(F.lds + YB_OFF + (blk & 1) * YB_BYTES);
;                 const unsigned aK = (unsigned)(size_t)(sb) + kap * 16, aVo = (unsigned)(size_t)(sb) + 5 * (SB * 256) + rown * 4, aVt = (unsigned)(size_t)(sb) + 5 * (SB * 256) + roth * 4;
;                 f32x4 cw, ca, cb, ck, cr; float cvo, cvt;
;     ...
;                 P4_RDSET(c, aK, 0, aVo, aVt, 0);
;                 asm volatile("s_waitcnt lgkmcnt(0)" : P4_TIE(c));
;                 {
;                     float ykeep = 0.f; const unsigned aK0 = aK, aVo0 = aVo, aVt0 = aVt;
.LBB0_489:
	s_and_b32 s3, s2, 1
	s_mul_i32 s22, s3, 0xb000
	v_lshl_add_u32 v78, s3, 12, v155
	v_lshl_add_u32 v197, s3, 12, v196
	s_add_i32 s3, s22, 0
	v_add_u32_e32 v79, s3, v91
	s_add_i32 s3, s3, 0xa000
	v_add_u32_e32 v80, s3, v99
	v_add_u32_e32 v81, s3, v103
	ds_read_b128 v[82:85], v79 offset:0
	ds_read_b128 v[86:89], v79 offset:0x2000
	ds_read_b128 v[114:117], v79 offset:0x4000
	ds_read_b128 v[118:121], v79 offset:0x6000
	ds_read_b128 v[122:125], v79 offset:0x8000
	ds_read_b32 v126, v80 offset:0
	ds_read_b32 v127, v81 offset:0
	s_add_i32 s2, s2, 1
	s_waitcnt lgkmcnt(0)
	ds_read_b128 v[162:165], v79 offset:0x100
	ds_read_b128 v[166:169], v79 offset:0x2100
	ds_read_b128 v[170:173], v79 offset:0x4100
	ds_read_b128 v[174:177], v79 offset:0x6100
	ds_read_b128 v[178:181], v79 offset:0x8100
	ds_read_b32 v182, v80 offset:0x80
	ds_read_b32 v183, v81 offset:0x80
	v_pk_mul_f32 v[250:251], v[70:71], v[86:87] op_sel_hi:[1,0]
	v_pk_fma_f32 v[250:251], v[72:73], v[86:87], v[250:251] op_sel:[0,1,0] op_sel_hi:[1,1,1]
	v_pk_fma_f32 v[250:251], v[74:75], v[88:89], v[250:251] op_sel_hi:[1,0,1]
	v_pk_fma_f32 v[250:251], v[76:77], v[88:89], v[250:251] op_sel:[0,1,0] op_sel_hi:[1,1,1]
	v_pk_mul_f32 v[184:185], v[126:127], v[118:119] op_sel_hi:[1,0]
	v_pk_mul_f32 v[186:187], v[126:127], v[118:119] op_sel:[0,1] op_sel_hi:[1,1]
	v_add_f32_dpp v252, v251, v250 quad_perm:[1,0,3,2] row_mask:0xf bank_mask:0xf bound_ctrl:1
	s_nop 0
	v_pk_mul_f32 v[188:189], v[126:127], v[120:121] op_sel_hi:[1,0]
	v_add_f32_dpp v252, v252, v252 quad_perm:[2,3,0,1] row_mask:0xf bank_mask:0xf bound_ctrl:1
	s_nop 0
	v_pk_mul_f32 v[190:191], v[126:127], v[120:121] op_sel:[0,1] op_sel_hi:[1,1]
	v_add_f32_dpp v252, v252, v252 row_ror:4 row_mask:0xf bank_mask:0xf bound_ctrl:1
	s_nop 0
	v_pk_fma_f32 v[184:185], v[70:71], v[82:83], v[184:185] op_sel_hi:[1,0,1]
	v_add_f32_dpp v252, v252, v252 row_ror:8 row_mask:0xf bank_mask:0xf bound_ctrl:1
	s_nop 0
	v_pk_fma_f32 v[186:187], v[72:73], v[82:83], v[186:187] op_sel:[0,1,0] op_sel_hi:[1,1,1]
	v_mov_b32_dpp v253, v252 quad_perm:[1,0,3,2] row_mask:0xf bank_mask:0xf bound_ctrl:1
	v_pk_fma_f32 v[188:189], v[74:75], v[84:85], v[188:189] op_sel_hi:[1,0,1]
	v_pk_fma_f32 v[190:191], v[76:77], v[84:85], v[190:191] op_sel:[0,1,0] op_sel_hi:[1,1,1]
	v_pk_fma_f32 v[70:71], v[252:253], v[114:115], v[184:185] op_sel_hi:[1,0,1]
	v_pk_fma_f32 v[72:73], v[252:253], v[114:115], v[186:187] op_sel:[0,1,0] op_sel_hi:[1,1,1]
	v_pk_fma_f32 v[74:75], v[252:253], v[116:117], v[188:189] op_sel_hi:[1,0,1]
	v_pk_fma_f32 v[76:77], v[252:253], v[116:117], v[190:191] op_sel:[0,1,0] op_sel_hi:[1,1,1]
	v_pk_mul_f32 v[192:193], v[70:71], v[122:123] op_sel_hi:[1,0]
	v_pk_fma_f32 v[192:193], v[72:73], v[122:123], v[192:193] op_sel:[0,1,0] op_sel_hi:[1,1,1]
	v_pk_fma_f32 v[192:193], v[74:75], v[124:125], v[192:193] op_sel_hi:[1,0,1]
	v_pk_fma_f32 v[192:193], v[76:77], v[124:125], v[192:193] op_sel:[0,1,0] op_sel_hi:[1,1,1]

	s_cmpk_lg_i32 s2, 0x88
	s_waitcnt lgkmcnt(0)
	s_nop 0
	ds_read_b128 v[82:85], v79 offset:0x200
	ds_read_b128 v[86:89], v79 offset:0x2200
	ds_read_b128 v[114:117], v79 offset:0x4200
	ds_read_b128 v[118:121], v79 offset:0x6200
	ds_read_b128 v[122:125], v79 offset:0x8200
	ds_read_b32 v126, v80 offset:0x100
	ds_read_b32 v127, v81 offset:0x100
	v_pk_mul_f32 v[250:251], v[70:71], v[166:167] op_sel_hi:[1,0]
	v_pk_fma_f32 v[250:251], v[72:73], v[166:167], v[250:251] op_sel:[0,1,0] op_sel_hi:[1,1,1]
	v_pk_fma_f32 v[250:251], v[74:75], v[168:169], v[250:251] op_sel_hi:[1,0,1]
	v_pk_fma_f32 v[250:251], v[76:77], v[168:169], v[250:251] op_sel:[0,1,0] op_sel_hi:[1,1,1]
	v_pk_mul_f32 v[184:185], v[182:183], v[174:175] op_sel_hi:[1,0]
	v_pk_mul_f32 v[186:187], v[182:183], v[174:175] op_sel:[0,1] op_sel_hi:[1,1]
	v_add_f32_dpp v252, v251, v250 quad_perm:[1,0,3,2] row_mask:0xf bank_mask:0xf bound_ctrl:1
	v_add_f32_dpp v92, v193, v192 quad_perm:[1,0,3,2] row_mask:0xf bank_mask:0xf bound_ctrl:1
	v_pk_mul_f32 v[188:189], v[182:183], v[176:177] op_sel_hi:[1,0]
	v_add_f32_dpp v252, v252, v252 quad_perm:[2,3,0,1] row_mask:0xf bank_mask:0xf bound_ctrl:1
	v_add_f32_dpp v92, v92, v92 quad_perm:[2,3,0,1] row_mask:0xf bank_mask:0xf bound_ctrl:1
	v_pk_mul_f32 v[190:191], v[182:183], v[176:177] op_sel:[0,1] op_sel_hi:[1,1]
	v_add_f32_dpp v252, v252, v252 row_ror:4 row_mask:0xf bank_mask:0xf bound_ctrl:1
	v_add_f32_dpp v92, v92, v92 row_ror:4 row_mask:0xf bank_mask:0xf bound_ctrl:1
	v_pk_fma_f32 v[184:185], v[70:71], v[162:163], v[184:185] op_sel_hi:[1,0,1]
	v_add_f32_dpp v252, v252, v252 row_ror:8 row_mask:0xf bank_mask:0xf bound_ctrl:1
	v_add_f32_dpp v92, v92, v92 row_ror:8 row_mask:0xf bank_mask:0x1 bound_ctrl:1
	v_pk_fma_f32 v[186:187], v[72:73], v[162:163], v[186:187] op_sel:[0,1,0] op_sel_hi:[1,1,1]
	v_mov_b32_dpp v253, v252 quad_perm:[1,0,3,2] row_mask:0xf bank_mask:0xf bound_ctrl:1
	v_pk_fma_f32 v[188:189], v[74:75], v[164:165], v[188:189] op_sel_hi:[1,0,1]
	v_pk_fma_f32 v[190:191], v[76:77], v[164:165], v[190:191] op_sel:[0,1,0] op_sel_hi:[1,1,1]
	v_pk_fma_f32 v[70:71], v[252:253], v[170:171], v[184:185] op_sel_hi:[1,0,1]
	v_pk_fma_f32 v[72:73], v[252:253], v[170:171], v[186:187] op_sel:[0,1,0] op_sel_hi:[1,1,1]
	v_pk_fma_f32 v[74:75], v[252:253], v[172:173], v[188:189] op_sel_hi:[1,0,1]
	v_pk_fma_f32 v[76:77], v[252:253], v[172:173], v[190:191] op_sel:[0,1,0] op_sel_hi:[1,1,1]
	v_pk_mul_f32 v[194:195], v[70:71], v[178:179] op_sel_hi:[1,0]
	v_pk_fma_f32 v[194:195], v[72:73], v[178:179], v[194:195] op_sel:[0,1,0] op_sel_hi:[1,1,1]
	v_pk_fma_f32 v[194:195], v[74:75], v[180:181], v[194:195] op_sel_hi:[1,0,1]
	v_pk_fma_f32 v[194:195], v[76:77], v[180:181], v[194:195] op_sel:[0,1,0] op_sel_hi:[1,1,1]

	s_waitcnt lgkmcnt(0)
	ds_read_b128 v[162:165], v79 offset:0x300
	ds_read_b128 v[166:169], v79 offset:0x2300
	ds_read_b128 v[170:173], v79 offset:0x4300
	ds_read_b128 v[174:177], v79 offset:0x6300
	ds_read_b128 v[178:181], v79 offset:0x8300
	ds_read_b32 v182, v80 offset:0x180
	ds_read_b32 v183, v81 offset:0x180
	v_pk_mul_f32 v[250:251], v[70:71], v[86:87] op_sel_hi:[1,0]
	v_pk_fma_f32 v[250:251], v[72:73], v[86:87], v[250:251] op_sel:[0,1,0] op_sel_hi:[1,1,1]
	v_pk_fma_f32 v[250:251], v[74:75], v[88:89], v[250:251] op_sel_hi:[1,0,1]
	v_pk_fma_f32 v[250:251], v[76:77], v[88:89], v[250:251] op_sel:[0,1,0] op_sel_hi:[1,1,1]
	v_pk_mul_f32 v[184:185], v[126:127], v[118:119] op_sel_hi:[1,0]
	v_pk_mul_f32 v[186:187], v[126:127], v[118:119] op_sel:[0,1] op_sel_hi:[1,1]
	v_add_f32_dpp v252, v251, v250 quad_perm:[1,0,3,2] row_mask:0xf bank_mask:0xf bound_ctrl:1
	v_add_f32_dpp v161, v195, v194 quad_perm:[1,0,3,2] row_mask:0xf bank_mask:0xf bound_ctrl:1
	v_pk_mul_f32 v[188:189], v[126:127], v[120:121] op_sel_hi:[1,0]
	v_add_f32_dpp v252, v252, v252 quad_perm:[2,3,0,1] row_mask:0xf bank_mask:0xf bound_ctrl:1
	v_add_f32_dpp v161, v161, v161 quad_perm:[2,3,0,1] row_mask:0xf bank_mask:0xf bound_ctrl:1
	v_pk_mul_f32 v[190:191], v[126:127], v[120:121] op_sel:[0,1] op_sel_hi:[1,1]
	v_add_f32_dpp v252, v252, v252 row_ror:4 row_mask:0xf bank_mask:0xf bound_ctrl:1
	v_add_f32_dpp v161, v161, v161 row_ror:4 row_mask:0xf bank_mask:0xf bound_ctrl:1
	v_pk_fma_f32 v[184:185], v[70:71], v[82:83], v[184:185] op_sel_hi:[1,0,1]
	v_add_f32_dpp v252, v252, v252 row_ror:8 row_mask:0xf bank_mask:0xf bound_ctrl:1
	v_add_f32_dpp v92, v161, v161 row_ror:8 row_mask:0xf bank_mask:0x2 bound_ctrl:1
	v_pk_fma_f32 v[186:187], v[72:73], v[82:83], v[186:187] op_sel:[0,1,0] op_sel_hi:[1,1,1]
	v_mov_b32_dpp v253, v252 quad_perm:[1,0,3,2] row_mask:0xf bank_mask:0xf bound_ctrl:1
	v_pk_fma_f32 v[188:189], v[74:75], v[84:85], v[188:189] op_sel_hi:[1,0,1]
	v_pk_fma_f32 v[190:191], v[76:77], v[84:85], v[190:191] op_sel:[0,1,0] op_sel_hi:[1,1,1]
	v_pk_fma_f32 v[70:71], v[252:253], v[114:115], v[184:185] op_sel_hi:[1,0,1]
	v_pk_fma_f32 v[72:73], v[252:253], v[114:115], v[186:187] op_sel:[0,1,0] op_sel_hi:[1,1,1]
	v_pk_fma_f32 v[74:75], v[252:253], v[116:117], v[188:189] op_sel_hi:[1,0,1]
	v_pk_fma_f32 v[76:77], v[252:253], v[116:117], v[190:191] op_sel:[0,1,0] op_sel_hi:[1,1,1]
	v_pk_mul_f32 v[192:193], v[70:71], v[122:123] op_sel_hi:[1,0]
	v_pk_fma_f32 v[192:193], v[72:73], v[122:123], v[192:193] op_sel:[0,1,0] op_sel_hi:[1,1,1]
	v_pk_fma_f32 v[192:193], v[74:75], v[124:125], v[192:193] op_sel_hi:[1,0,1]
	v_pk_fma_f32 v[192:193], v[76:77], v[124:125], v[192:193] op_sel:[0,1,0] op_sel_hi:[1,1,1]

	s_waitcnt lgkmcnt(0)
	ds_read_b128 v[82:85], v79 offset:0x400
	ds_read_b128 v[86:89], v79 offset:0x2400
	ds_read_b128 v[114:117], v79 offset:0x4400
	ds_read_b128 v[118:121], v79 offset:0x6400
	ds_read_b128 v[122:125], v79 offset:0x8400
	ds_read_b32 v126, v80 offset:0x200
	ds_read_b32 v127, v81 offset:0x200
	v_pk_mul_f32 v[250:251], v[70:71], v[166:167] op_sel_hi:[1,0]
	v_pk_fma_f32 v[250:251], v[72:73], v[166:167], v[250:251] op_sel:[0,1,0] op_sel_hi:[1,1,1]
	v_pk_fma_f32 v[250:251], v[74:75], v[168:169], v[250:251] op_sel_hi:[1,0,1]
	v_pk_fma_f32 v[250:251], v[76:77], v[168:169], v[250:251] op_sel:[0,1,0] op_sel_hi:[1,1,1]
	v_pk_mul_f32 v[184:185], v[182:183], v[174:175] op_sel_hi:[1,0]
	v_pk_mul_f32 v[186:187], v[182:183], v[174:175] op_sel:[0,1] op_sel_hi:[1,1]
	v_add_f32_dpp v252, v251, v250 quad_perm:[1,0,3,2] row_mask:0xf bank_mask:0xf bound_ctrl:1
	v_add_f32_dpp v161, v193, v192 quad_perm:[1,0,3,2] row_mask:0xf bank_mask:0xf bound_ctrl:1
	v_pk_mul_f32 v[188:189], v[182:183], v[176:177] op_sel_hi:[1,0]
	v_add_f32_dpp v252, v252, v252 quad_perm:[2,3,0,1] row_mask:0xf bank_mask:0xf bound_ctrl:1
	v_add_f32_dpp v161, v161, v161 quad_perm:[2,3,0,1] row_mask:0xf bank_mask:0xf bound_ctrl:1
	v_pk_mul_f32 v[190:191], v[182:183], v[176:177] op_sel:[0,1] op_sel_hi:[1,1]
	v_add_f32_dpp v252, v252, v252 row_ror:4 row_mask:0xf bank_mask:0xf bound_ctrl:1
	v_add_f32_dpp v161, v161, v161 row_ror:4 row_mask:0xf bank_mask:0xf bound_ctrl:1
	v_pk_fma_f32 v[184:185], v[70:71], v[162:163], v[184:185] op_sel_hi:[1,0,1]
	v_add_f32_dpp v252, v252, v252 row_ror:8 row_mask:0xf bank_mask:0xf bound_ctrl:1
	v_add_f32_dpp v92, v161, v161 row_ror:8 row_mask:0xf bank_mask:0x4 bound_ctrl:1
	v_pk_fma_f32 v[186:187], v[72:73], v[162:163], v[186:187] op_sel:[0,1,0] op_sel_hi:[1,1,1]
	v_mov_b32_dpp v253, v252 quad_perm:[1,0,3,2] row_mask:0xf bank_mask:0xf bound_ctrl:1
	v_pk_fma_f32 v[188:189], v[74:75], v[164:165], v[188:189] op_sel_hi:[1,0,1]
	v_pk_fma_f32 v[190:191], v[76:77], v[164:165], v[190:191] op_sel:[0,1,0] op_sel_hi:[1,1,1]
	v_pk_fma_f32 v[70:71], v[252:253], v[170:171], v[184:185] op_sel_hi:[1,0,1]
	v_pk_fma_f32 v[72:73], v[252:253], v[170:171], v[186:187] op_sel:[0,1,0] op_sel_hi:[1,1,1]
	v_pk_fma_f32 v[74:75], v[252:253], v[172:173], v[188:189] op_sel_hi:[1,0,1]
	v_pk_fma_f32 v[76:77], v[252:253], v[172:173], v[190:191] op_sel:[0,1,0] op_sel_hi:[1,1,1]
	v_pk_mul_f32 v[194:195], v[70:71], v[178:179] op_sel_hi:[1,0]
	v_pk_fma_f32 v[194:195], v[72:73], v[178:179], v[194:195] op_sel:[0,1,0] op_sel_hi:[1,1,1]
	v_pk_fma_f32 v[194:195], v[74:75], v[180:181], v[194:195] op_sel_hi:[1,0,1]
	v_pk_fma_f32 v[194:195], v[76:77], v[180:181], v[194:195] op_sel:[0,1,0] op_sel_hi:[1,1,1]

	s_waitcnt lgkmcnt(0)
	ds_read_b128 v[162:165], v79 offset:0x500
	ds_read_b128 v[166:169], v79 offset:0x2500
	ds_read_b128 v[170:173], v79 offset:0x4500
	ds_read_b128 v[174:177], v79 offset:0x6500
	ds_read_b128 v[178:181], v79 offset:0x8500
	ds_read_b32 v182, v80 offset:0x280
	ds_read_b32 v183, v81 offset:0x280
	v_pk_mul_f32 v[250:251], v[70:71], v[86:87] op_sel_hi:[1,0]
	v_pk_fma_f32 v[250:251], v[72:73], v[86:87], v[250:251] op_sel:[0,1,0] op_sel_hi:[1,1,1]
	v_pk_fma_f32 v[250:251], v[74:75], v[88:89], v[250:251] op_sel_hi:[1,0,1]
	v_pk_fma_f32 v[250:251], v[76:77], v[88:89], v[250:251] op_sel:[0,1,0] op_sel_hi:[1,1,1]
	v_pk_mul_f32 v[184:185], v[126:127], v[118:119] op_sel_hi:[1,0]
	v_pk_mul_f32 v[186:187], v[126:127], v[118:119] op_sel:[0,1] op_sel_hi:[1,1]
	v_add_f32_dpp v252, v251, v250 quad_perm:[1,0,3,2] row_mask:0xf bank_mask:0xf bound_ctrl:1
	v_add_f32_dpp v161, v195, v194 quad_perm:[1,0,3,2] row_mask:0xf bank_mask:0xf bound_ctrl:1
	v_pk_mul_f32 v[188:189], v[126:127], v[120:121] op_sel_hi:[1,0]
	v_add_f32_dpp v252, v252, v252 quad_perm:[2,3,0,1] row_mask:0xf bank_mask:0xf bound_ctrl:1
	v_add_f32_dpp v161, v161, v161 quad_perm:[2,3,0,1] row_mask:0xf bank_mask:0xf bound_ctrl:1
	v_pk_mul_f32 v[190:191], v[126:127], v[120:121] op_sel:[0,1] op_sel_hi:[1,1]
	v_add_f32_dpp v252, v252, v252 row_ror:4 row_mask:0xf bank_mask:0xf bound_ctrl:1
	v_add_f32_dpp v161, v161, v161 row_ror:4 row_mask:0xf bank_mask:0xf bound_ctrl:1
	v_pk_fma_f32 v[184:185], v[70:71], v[82:83], v[184:185] op_sel_hi:[1,0,1]
	v_add_f32_dpp v252, v252, v252 row_ror:8 row_mask:0xf bank_mask:0xf bound_ctrl:1
	v_add_f32_dpp v92, v161, v161 row_ror:8 row_mask:0xf bank_mask:0x8 bound_ctrl:1
	v_pk_fma_f32 v[186:187], v[72:73], v[82:83], v[186:187] op_sel:[0,1,0] op_sel_hi:[1,1,1]
	v_mov_b32_dpp v253, v252 quad_perm:[1,0,3,2] row_mask:0xf bank_mask:0xf bound_ctrl:1
	v_pk_fma_f32 v[188:189], v[74:75], v[84:85], v[188:189] op_sel_hi:[1,0,1]
	v_pk_fma_f32 v[190:191], v[76:77], v[84:85], v[190:191] op_sel:[0,1,0] op_sel_hi:[1,1,1]
	v_pk_fma_f32 v[70:71], v[252:253], v[114:115], v[184:185] op_sel_hi:[1,0,1]
	v_pk_fma_f32 v[72:73], v[252:253], v[114:115], v[186:187] op_sel:[0,1,0] op_sel_hi:[1,1,1]
	v_pk_fma_f32 v[74:75], v[252:253], v[116:117], v[188:189] op_sel_hi:[1,0,1]
	v_pk_fma_f32 v[76:77], v[252:253], v[116:117], v[190:191] op_sel:[0,1,0] op_sel_hi:[1,1,1]
	v_pk_mul_f32 v[192:193], v[70:71], v[122:123] op_sel_hi:[1,0]
	v_pk_fma_f32 v[192:193], v[72:73], v[122:123], v[192:193] op_sel:[0,1,0] op_sel_hi:[1,1,1]
	v_pk_fma_f32 v[192:193], v[74:75], v[124:125], v[192:193] op_sel_hi:[1,0,1]
	v_pk_fma_f32 v[192:193], v[76:77], v[124:125], v[192:193] op_sel:[0,1,0] op_sel_hi:[1,1,1]

	s_waitcnt lgkmcnt(0)
	ds_write_b32 v197, v92 offset:0
	ds_read_b128 v[82:85], v79 offset:0x600
	ds_read_b128 v[86:89], v79 offset:0x2600
	ds_read_b128 v[114:117], v79 offset:0x4600
	ds_read_b128 v[118:121], v79 offset:0x6600
	ds_read_b128 v[122:125], v79 offset:0x8600
	ds_read_b32 v126, v80 offset:0x300
	ds_read_b32 v127, v81 offset:0x300
	v_pk_mul_f32 v[250:251], v[70:71], v[166:167] op_sel_hi:[1,0]
	v_pk_fma_f32 v[250:251], v[72:73], v[166:167], v[250:251] op_sel:[0,1,0] op_sel_hi:[1,1,1]
	v_pk_fma_f32 v[250:251], v[74:75], v[168:169], v[250:251] op_sel_hi:[1,0,1]
	v_pk_fma_f32 v[250:251], v[76:77], v[168:169], v[250:251] op_sel:[0,1,0] op_sel_hi:[1,1,1]
	v_pk_mul_f32 v[184:185], v[182:183], v[174:175] op_sel_hi:[1,0]
	v_pk_mul_f32 v[186:187], v[182:183], v[174:175] op_sel:[0,1] op_sel_hi:[1,1]
	v_add_f32_dpp v252, v251, v250 quad_perm:[1,0,3,2] row_mask:0xf bank_mask:0xf bound_ctrl:1
	v_add_f32_dpp v161, v193, v192 quad_perm:[1,0,3,2] row_mask:0xf bank_mask:0xf bound_ctrl:1
	v_pk_mul_f32 v[188:189], v[182:183], v[176:177] op_sel_hi:[1,0]
	v_add_f32_dpp v252, v252, v252 quad_perm:[2,3,0,1] row_mask:0xf bank_mask:0xf bound_ctrl:1
	v_add_f32_dpp v161, v161, v161 quad_perm:[2,3,0,1] row_mask:0xf bank_mask:0xf bound_ctrl:1
	v_pk_mul_f32 v[190:191], v[182:183], v[176:177] op_sel:[0,1] op_sel_hi:[1,1]
	v_add_f32_dpp v252, v252, v252 row_ror:4 row_mask:0xf bank_mask:0xf bound_ctrl:1
	v_add_f32_dpp v161, v161, v161 row_ror:4 row_mask:0xf bank_mask:0xf bound_ctrl:1
	v_pk_fma_f32 v[184:185], v[70:71], v[162:163], v[184:185] op_sel_hi:[1,0,1]
	v_add_f32_dpp v252, v252, v252 row_ror:8 row_mask:0xf bank_mask:0xf bound_ctrl:1
	v_add_f32_dpp v92, v161, v161 row_ror:8 row_mask:0xf bank_mask:0x1 bound_ctrl:1
	v_pk_fma_f32 v[186:187], v[72:73], v[162:163], v[186:187] op_sel:[0,1,0] op_sel_hi:[1,1,1]
	v_mov_b32_dpp v253, v252 quad_perm:[1,0,3,2] row_mask:0xf bank_mask:0xf bound_ctrl:1
	v_pk_fma_f32 v[188:189], v[74:75], v[164:165], v[188:189] op_sel_hi:[1,0,1]
	v_pk_fma_f32 v[190:191], v[76:77], v[164:165], v[190:191] op_sel:[0,1,0] op_sel_hi:[1,1,1]
	v_pk_fma_f32 v[70:71], v[252:253], v[170:171], v[184:185] op_sel_hi:[1,0,1]
	v_pk_fma_f32 v[72:73], v[252:253], v[170:171], v[186:187] op_sel:[0,1,0] op_sel_hi:[1,1,1]
	v_pk_fma_f32 v[74:75], v[252:253], v[172:173], v[188:189] op_sel_hi:[1,0,1]
	v_pk_fma_f32 v[76:77], v[252:253], v[172:173], v[190:191] op_sel:[0,1,0] op_sel_hi:[1,1,1]
	v_pk_mul_f32 v[194:195], v[70:71], v[178:179] op_sel_hi:[1,0]
	v_pk_fma_f32 v[194:195], v[72:73], v[178:179], v[194:195] op_sel:[0,1,0] op_sel_hi:[1,1,1]
	v_pk_fma_f32 v[194:195], v[74:75], v[180:181], v[194:195] op_sel_hi:[1,0,1]
	v_pk_fma_f32 v[194:195], v[76:77], v[180:181], v[194:195] op_sel:[0,1,0] op_sel_hi:[1,1,1]

	s_waitcnt lgkmcnt(0)
	ds_read_b128 v[162:165], v79 offset:0x700
	ds_read_b128 v[166:169], v79 offset:0x2700
	ds_read_b128 v[170:173], v79 offset:0x4700
	ds_read_b128 v[174:177], v79 offset:0x6700
	ds_read_b128 v[178:181], v79 offset:0x8700
	ds_read_b32 v182, v80 offset:0x380
	ds_read_b32 v183, v81 offset:0x380
	v_pk_mul_f32 v[250:251], v[70:71], v[86:87] op_sel_hi:[1,0]
	v_pk_fma_f32 v[250:251], v[72:73], v[86:87], v[250:251] op_sel:[0,1,0] op_sel_hi:[1,1,1]
	v_pk_fma_f32 v[250:251], v[74:75], v[88:89], v[250:251] op_sel_hi:[1,0,1]
	v_pk_fma_f32 v[250:251], v[76:77], v[88:89], v[250:251] op_sel:[0,1,0] op_sel_hi:[1,1,1]
	v_pk_mul_f32 v[184:185], v[126:127], v[118:119] op_sel_hi:[1,0]
	v_pk_mul_f32 v[186:187], v[126:127], v[118:119] op_sel:[0,1] op_sel_hi:[1,1]
	v_add_f32_dpp v252, v251, v250 quad_perm:[1,0,3,2] row_mask:0xf bank_mask:0xf bound_ctrl:1
	v_add_f32_dpp v161, v195, v194 quad_perm:[1,0,3,2] row_mask:0xf bank_mask:0xf bound_ctrl:1
	v_pk_mul_f32 v[188:189], v[126:127], v[120:121] op_sel_hi:[1,0]
	v_add_f32_dpp v252, v252, v252 quad_perm:[2,3,0,1] row_mask:0xf bank_mask:0xf bound_ctrl:1
	v_add_f32_dpp v161, v161, v161 quad_perm:[2,3,0,1] row_mask:0xf bank_mask:0xf bound_ctrl:1
	v_pk_mul_f32 v[190:191], v[126:127], v[120:121] op_sel:[0,1] op_sel_hi:[1,1]
	v_add_f32_dpp v252, v252, v252 row_ror:4 row_mask:0xf bank_mask:0xf bound_ctrl:1
	v_add_f32_dpp v161, v161, v161 row_ror:4 row_mask:0xf bank_mask:0xf bound_ctrl:1
	v_pk_fma_f32 v[184:185], v[70:71], v[82:83], v[184:185] op_sel_hi:[1,0,1]
	v_add_f32_dpp v252, v252, v252 row_ror:8 row_mask:0xf bank_mask:0xf bound_ctrl:1
	v_add_f32_dpp v92, v161, v161 row_ror:8 row_mask:0xf bank_mask:0x2 bound_ctrl:1
	v_pk_fma_f32 v[186:187], v[72:73], v[82:83], v[186:187] op_sel:[0,1,0] op_sel_hi:[1,1,1]
	v_mov_b32_dpp v253, v252 quad_perm:[1,0,3,2] row_mask:0xf bank_mask:0xf bound_ctrl:1
	v_pk_fma_f32 v[188:189], v[74:75], v[84:85], v[188:189] op_sel_hi:[1,0,1]
	v_pk_fma_f32 v[190:191], v[76:77], v[84:85], v[190:191] op_sel:[0,1,0] op_sel_hi:[1,1,1]
	v_pk_fma_f32 v[70:71], v[252:253], v[114:115], v[184:185] op_sel_hi:[1,0,1]
	v_pk_fma_f32 v[72:73], v[252:253], v[114:115], v[186:187] op_sel:[0,1,0] op_sel_hi:[1,1,1]
	v_pk_fma_f32 v[74:75], v[252:253], v[116:117], v[188:189] op_sel_hi:[1,0,1]
	v_pk_fma_f32 v[76:77], v[252:253], v[116:117], v[190:191] op_sel:[0,1,0] op_sel_hi:[1,1,1]
	v_pk_mul_f32 v[192:193], v[70:71], v[122:123] op_sel_hi:[1,0]
	v_pk_fma_f32 v[192:193], v[72:73], v[122:123], v[192:193] op_sel:[0,1,0] op_sel_hi:[1,1,1]
	v_pk_fma_f32 v[192:193], v[74:75], v[124:125], v[192:193] op_sel_hi:[1,0,1]
	v_pk_fma_f32 v[192:193], v[76:77], v[124:125], v[192:193] op_sel:[0,1,0] op_sel_hi:[1,1,1]

	s_waitcnt lgkmcnt(0)
	ds_read_b128 v[82:85], v79 offset:0x800
	ds_read_b128 v[86:89], v79 offset:0x2800
	ds_read_b128 v[114:117], v79 offset:0x4800
	ds_read_b128 v[118:121], v79 offset:0x6800
	ds_read_b128 v[122:125], v79 offset:0x8800
	ds_read_b32 v126, v80 offset:0x400
	ds_read_b32 v127, v81 offset:0x400
	v_pk_mul_f32 v[250:251], v[70:71], v[166:167] op_sel_hi:[1,0]
	v_pk_fma_f32 v[250:251], v[72:73], v[166:167], v[250:251] op_sel:[0,1,0] op_sel_hi:[1,1,1]
	v_pk_fma_f32 v[250:251], v[74:75], v[168:169], v[250:251] op_sel_hi:[1,0,1]
	v_pk_fma_f32 v[250:251], v[76:77], v[168:169], v[250:251] op_sel:[0,1,0] op_sel_hi:[1,1,1]
	v_pk_mul_f32 v[184:185], v[182:183], v[174:175] op_sel_hi:[1,0]
	v_pk_mul_f32 v[186:187], v[182:183], v[174:175] op_sel:[0,1] op_sel_hi:[1,1]
	v_add_f32_dpp v252, v251, v250 quad_perm:[1,0,3,2] row_mask:0xf bank_mask:0xf bound_ctrl:1
	v_add_f32_dpp v161, v193, v192 quad_perm:[1,0,3,2] row_mask:0xf bank_mask:0xf bound_ctrl:1
	v_pk_mul_f32 v[188:189], v[182:183], v[176:177] op_sel_hi:[1,0]
	v_add_f32_dpp v252, v252, v252 quad_perm:[2,3,0,1] row_mask:0xf bank_mask:0xf bound_ctrl:1
	v_add_f32_dpp v161, v161, v161 quad_perm:[2,3,0,1] row_mask:0xf bank_mask:0xf bound_ctrl:1
	v_pk_mul_f32 v[190:191], v[182:183], v[176:177] op_sel:[0,1] op_sel_hi:[1,1]
	v_add_f32_dpp v252, v252, v252 row_ror:4 row_mask:0xf bank_mask:0xf bound_ctrl:1
	v_add_f32_dpp v161, v161, v161 row_ror:4 row_mask:0xf bank_mask:0xf bound_ctrl:1
	v_pk_fma_f32 v[184:185], v[70:71], v[162:163], v[184:185] op_sel_hi:[1,0,1]
	v_add_f32_dpp v252, v252, v252 row_ror:8 row_mask:0xf bank_mask:0xf bound_ctrl:1
	v_add_f32_dpp v92, v161, v161 row_ror:8 row_mask:0xf bank_mask:0x4 bound_ctrl:1
	v_pk_fma_f32 v[186:187], v[72:73], v[162:163], v[186:187] op_sel:[0,1,0] op_sel_hi:[1,1,1]
	v_mov_b32_dpp v253, v252 quad_perm:[1,0,3,2] row_mask:0xf bank_mask:0xf bound_ctrl:1
	v_pk_fma_f32 v[188:189], v[74:75], v[164:165], v[188:189] op_sel_hi:[1,0,1]
	v_pk_fma_f32 v[190:191], v[76:77], v[164:165], v[190:191] op_sel:[0,1,0] op_sel_hi:[1,1,1]
	v_pk_fma_f32 v[70:71], v[252:253], v[170:171], v[184:185] op_sel_hi:[1,0,1]
	v_pk_fma_f32 v[72:73], v[252:253], v[170:171], v[186:187] op_sel:[0,1,0] op_sel_hi:[1,1,1]
	v_pk_fma_f32 v[74:75], v[252:253], v[172:173], v[188:189] op_sel_hi:[1,0,1]
	v_pk_fma_f32 v[76:77], v[252:253], v[172:173], v[190:191] op_sel:[0,1,0] op_sel_hi:[1,1,1]
	v_pk_mul_f32 v[194:195], v[70:71], v[178:179] op_sel_hi:[1,0]
	v_pk_fma_f32 v[194:195], v[72:73], v[178:179], v[194:195] op_sel:[0,1,0] op_sel_hi:[1,1,1]
	v_pk_fma_f32 v[194:195], v[74:75], v[180:181], v[194:195] op_sel_hi:[1,0,1]
	v_pk_fma_f32 v[194:195], v[76:77], v[180:181], v[194:195] op_sel:[0,1,0] op_sel_hi:[1,1,1]

	s_waitcnt lgkmcnt(0)
	ds_read_b128 v[162:165], v79 offset:0x900
	ds_read_b128 v[166:169], v79 offset:0x2900
	ds_read_b128 v[170:173], v79 offset:0x4900
	ds_read_b128 v[174:177], v79 offset:0x6900
	ds_read_b128 v[178:181], v79 offset:0x8900
	ds_read_b32 v182, v80 offset:0x480
	ds_read_b32 v183, v81 offset:0x480
	v_pk_mul_f32 v[250:251], v[70:71], v[86:87] op_sel_hi:[1,0]
	v_pk_fma_f32 v[250:251], v[72:73], v[86:87], v[250:251] op_sel:[0,1,0] op_sel_hi:[1,1,1]
	v_pk_fma_f32 v[250:251], v[74:75], v[88:89], v[250:251] op_sel_hi:[1,0,1]
	v_pk_fma_f32 v[250:251], v[76:77], v[88:89], v[250:251] op_sel:[0,1,0] op_sel_hi:[1,1,1]
	v_pk_mul_f32 v[184:185], v[126:127], v[118:119] op_sel_hi:[1,0]
	v_pk_mul_f32 v[186:187], v[126:127], v[118:119] op_sel:[0,1] op_sel_hi:[1,1]
	v_add_f32_dpp v252, v251, v250 quad_perm:[1,0,3,2] row_mask:0xf bank_mask:0xf bound_ctrl:1
	v_add_f32_dpp v161, v195, v194 quad_perm:[1,0,3,2] row_mask:0xf bank_mask:0xf bound_ctrl:1
	v_pk_mul_f32 v[188:189], v[126:127], v[120:121] op_sel_hi:[1,0]
	v_add_f32_dpp v252, v252, v252 quad_perm:[2,3,0,1] row_mask:0xf bank_mask:0xf bound_ctrl:1
	v_add_f32_dpp v161, v161, v161 quad_perm:[2,3,0,1] row_mask:0xf bank_mask:0xf bound_ctrl:1
	v_pk_mul_f32 v[190:191], v[126:127], v[120:121] op_sel:[0,1] op_sel_hi:[1,1]
	v_add_f32_dpp v252, v252, v252 row_ror:4 row_mask:0xf bank_mask:0xf bound_ctrl:1
	v_add_f32_dpp v161, v161, v161 row_ror:4 row_mask:0xf bank_mask:0xf bound_ctrl:1
	v_pk_fma_f32 v[184:185], v[70:71], v[82:83], v[184:185] op_sel_hi:[1,0,1]
	v_add_f32_dpp v252, v252, v252 row_ror:8 row_mask:0xf bank_mask:0xf bound_ctrl:1
	v_add_f32_dpp v92, v161, v161 row_ror:8 row_mask:0xf bank_mask:0x8 bound_ctrl:1
	v_pk_fma_f32 v[186:187], v[72:73], v[82:83], v[186:187] op_sel:[0,1,0] op_sel_hi:[1,1,1]
	v_mov_b32_dpp v253, v252 quad_perm:[1,0,3,2] row_mask:0xf bank_mask:0xf bound_ctrl:1
	v_pk_fma_f32 v[188:189], v[74:75], v[84:85], v[188:189] op_sel_hi:[1,0,1]
	v_pk_fma_f32 v[190:191], v[76:77], v[84:85], v[190:191] op_sel:[0,1,0] op_sel_hi:[1,1,1]
	v_pk_fma_f32 v[70:71], v[252:253], v[114:115], v[184:185] op_sel_hi:[1,0,1]
	v_pk_fma_f32 v[72:73], v[252:253], v[114:115], v[186:187] op_sel:[0,1,0] op_sel_hi:[1,1,1]
	v_pk_fma_f32 v[74:75], v[252:253], v[116:117], v[188:189] op_sel_hi:[1,0,1]
	v_pk_fma_f32 v[76:77], v[252:253], v[116:117], v[190:191] op_sel:[0,1,0] op_sel_hi:[1,1,1]
	v_pk_mul_f32 v[192:193], v[70:71], v[122:123] op_sel_hi:[1,0]
	v_pk_fma_f32 v[192:193], v[72:73], v[122:123], v[192:193] op_sel:[0,1,0] op_sel_hi:[1,1,1]
	v_pk_fma_f32 v[192:193], v[74:75], v[124:125], v[192:193] op_sel_hi:[1,0,1]
	v_pk_fma_f32 v[192:193], v[76:77], v[124:125], v[192:193] op_sel:[0,1,0] op_sel_hi:[1,1,1]

	s_nop 0
	ds_write_b32 v197, v92 offset:512
	s_waitcnt lgkmcnt(0)
	s_nop 0
	ds_read_b128 v[82:85], v79 offset:0xa00
	ds_read_b128 v[86:89], v79 offset:0x2a00
	ds_read_b128 v[114:117], v79 offset:0x4a00
	ds_read_b128 v[118:121], v79 offset:0x6a00
	ds_read_b128 v[122:125], v79 offset:0x8a00
	ds_read_b32 v126, v80 offset:0x500
	ds_read_b32 v127, v81 offset:0x500
	v_pk_mul_f32 v[250:251], v[70:71], v[166:167] op_sel_hi:[1,0]
	v_pk_fma_f32 v[250:251], v[72:73], v[166:167], v[250:251] op_sel:[0,1,0] op_sel_hi:[1,1,1]
	v_pk_fma_f32 v[250:251], v[74:75], v[168:169], v[250:251] op_sel_hi:[1,0,1]
	v_pk_fma_f32 v[250:251], v[76:77], v[168:169], v[250:251] op_sel:[0,1,0] op_sel_hi:[1,1,1]
	v_pk_mul_f32 v[184:185], v[182:183], v[174:175] op_sel_hi:[1,0]
	v_pk_mul_f32 v[186:187], v[182:183], v[174:175] op_sel:[0,1] op_sel_hi:[1,1]
	v_add_f32_dpp v252, v251, v250 quad_perm:[1,0,3,2] row_mask:0xf bank_mask:0xf bound_ctrl:1
	v_add_f32_dpp v92, v193, v192 quad_perm:[1,0,3,2] row_mask:0xf bank_mask:0xf bound_ctrl:1
	v_pk_mul_f32 v[188:189], v[182:183], v[176:177] op_sel_hi:[1,0]
	v_add_f32_dpp v252, v252, v252 quad_perm:[2,3,0,1] row_mask:0xf bank_mask:0xf bound_ctrl:1
	v_add_f32_dpp v92, v92, v92 quad_perm:[2,3,0,1] row_mask:0xf bank_mask:0xf bound_ctrl:1
	v_pk_mul_f32 v[190:191], v[182:183], v[176:177] op_sel:[0,1] op_sel_hi:[1,1]
	v_add_f32_dpp v252, v252, v252 row_ror:4 row_mask:0xf bank_mask:0xf bound_ctrl:1
	v_add_f32_dpp v92, v92, v92 row_ror:4 row_mask:0xf bank_mask:0xf bound_ctrl:1
	v_pk_fma_f32 v[184:185], v[70:71], v[162:163], v[184:185] op_sel_hi:[1,0,1]
	v_add_f32_dpp v252, v252, v252 row_ror:8 row_mask:0xf bank_mask:0xf bound_ctrl:1
	v_add_f32_dpp v92, v92, v92 row_ror:8 row_mask:0xf bank_mask:0x1 bound_ctrl:1
	v_pk_fma_f32 v[186:187], v[72:73], v[162:163], v[186:187] op_sel:[0,1,0] op_sel_hi:[1,1,1]
	v_mov_b32_dpp v253, v252 quad_perm:[1,0,3,2] row_mask:0xf bank_mask:0xf bound_ctrl:1
	v_pk_fma_f32 v[188:189], v[74:75], v[164:165], v[188:189] op_sel_hi:[1,0,1]
	v_pk_fma_f32 v[190:191], v[76:77], v[164:165], v[190:191] op_sel:[0,1,0] op_sel_hi:[1,1,1]
	v_pk_fma_f32 v[70:71], v[252:253], v[170:171], v[184:185] op_sel_hi:[1,0,1]
	v_pk_fma_f32 v[72:73], v[252:253], v[170:171], v[186:187] op_sel:[0,1,0] op_sel_hi:[1,1,1]
	v_pk_fma_f32 v[74:75], v[252:253], v[172:173], v[188:189] op_sel_hi:[1,0,1]
	v_pk_fma_f32 v[76:77], v[252:253], v[172:173], v[190:191] op_sel:[0,1,0] op_sel_hi:[1,1,1]
	v_pk_mul_f32 v[194:195], v[70:71], v[178:179] op_sel_hi:[1,0]
	v_pk_fma_f32 v[194:195], v[72:73], v[178:179], v[194:195] op_sel:[0,1,0] op_sel_hi:[1,1,1]
	v_pk_fma_f32 v[194:195], v[74:75], v[180:181], v[194:195] op_sel_hi:[1,0,1]
	v_pk_fma_f32 v[194:195], v[76:77], v[180:181], v[194:195] op_sel:[0,1,0] op_sel_hi:[1,1,1]

	s_waitcnt lgkmcnt(0)
	ds_read_b128 v[162:165], v79 offset:0xb00
	ds_read_b128 v[166:169], v79 offset:0x2b00
	ds_read_b128 v[170:173], v79 offset:0x4b00
	ds_read_b128 v[174:177], v79 offset:0x6b00
	ds_read_b128 v[178:181], v79 offset:0x8b00
	ds_read_b32 v182, v80 offset:0x580
	ds_read_b32 v183, v81 offset:0x580
	v_pk_mul_f32 v[250:251], v[70:71], v[86:87] op_sel_hi:[1,0]
	v_pk_fma_f32 v[250:251], v[72:73], v[86:87], v[250:251] op_sel:[0,1,0] op_sel_hi:[1,1,1]
	v_pk_fma_f32 v[250:251], v[74:75], v[88:89], v[250:251] op_sel_hi:[1,0,1]
	v_pk_fma_f32 v[250:251], v[76:77], v[88:89], v[250:251] op_sel:[0,1,0] op_sel_hi:[1,1,1]
	v_pk_mul_f32 v[184:185], v[126:127], v[118:119] op_sel_hi:[1,0]
	v_pk_mul_f32 v[186:187], v[126:127], v[118:119] op_sel:[0,1] op_sel_hi:[1,1]
	v_add_f32_dpp v252, v251, v250 quad_perm:[1,0,3,2] row_mask:0xf bank_mask:0xf bound_ctrl:1
	v_add_f32_dpp v161, v195, v194 quad_perm:[1,0,3,2] row_mask:0xf bank_mask:0xf bound_ctrl:1
	v_pk_mul_f32 v[188:189], v[126:127], v[120:121] op_sel_hi:[1,0]
	v_add_f32_dpp v252, v252, v252 quad_perm:[2,3,0,1] row_mask:0xf bank_mask:0xf bound_ctrl:1
	v_add_f32_dpp v161, v161, v161 quad_perm:[2,3,0,1] row_mask:0xf bank_mask:0xf bound_ctrl:1
	v_pk_mul_f32 v[190:191], v[126:127], v[120:121] op_sel:[0,1] op_sel_hi:[1,1]
	v_add_f32_dpp v252, v252, v252 row_ror:4 row_mask:0xf bank_mask:0xf bound_ctrl:1
	v_add_f32_dpp v161, v161, v161 row_ror:4 row_mask:0xf bank_mask:0xf bound_ctrl:1
	v_pk_fma_f32 v[184:185], v[70:71], v[82:83], v[184:185] op_sel_hi:[1,0,1]
	v_add_f32_dpp v252, v252, v252 row_ror:8 row_mask:0xf bank_mask:0xf bound_ctrl:1
	v_add_f32_dpp v92, v161, v161 row_ror:8 row_mask:0xf bank_mask:0x2 bound_ctrl:1
	v_pk_fma_f32 v[186:187], v[72:73], v[82:83], v[186:187] op_sel:[0,1,0] op_sel_hi:[1,1,1]
	v_mov_b32_dpp v253, v252 quad_perm:[1,0,3,2] row_mask:0xf bank_mask:0xf bound_ctrl:1
	v_pk_fma_f32 v[188:189], v[74:75], v[84:85], v[188:189] op_sel_hi:[1,0,1]
	v_pk_fma_f32 v[190:191], v[76:77], v[84:85], v[190:191] op_sel:[0,1,0] op_sel_hi:[1,1,1]
	v_pk_fma_f32 v[70:71], v[252:253], v[114:115], v[184:185] op_sel_hi:[1,0,1]
	v_pk_fma_f32 v[72:73], v[252:253], v[114:115], v[186:187] op_sel:[0,1,0] op_sel_hi:[1,1,1]
	v_pk_fma_f32 v[74:75], v[252:253], v[116:117], v[188:189] op_sel_hi:[1,0,1]
	v_pk_fma_f32 v[76:77], v[252:253], v[116:117], v[190:191] op_sel:[0,1,0] op_sel_hi:[1,1,1]
	v_pk_mul_f32 v[192:193], v[70:71], v[122:123] op_sel_hi:[1,0]
	v_pk_fma_f32 v[192:193], v[72:73], v[122:123], v[192:193] op_sel:[0,1,0] op_sel_hi:[1,1,1]
	v_pk_fma_f32 v[192:193], v[74:75], v[124:125], v[192:193] op_sel_hi:[1,0,1]
	v_pk_fma_f32 v[192:193], v[76:77], v[124:125], v[192:193] op_sel:[0,1,0] op_sel_hi:[1,1,1]

	s_waitcnt lgkmcnt(0)
	ds_read_b128 v[82:85], v79 offset:0xc00
	ds_read_b128 v[86:89], v79 offset:0x2c00
	ds_read_b128 v[114:117], v79 offset:0x4c00
	ds_read_b128 v[118:121], v79 offset:0x6c00
	ds_read_b128 v[122:125], v79 offset:0x8c00
	ds_read_b32 v126, v80 offset:0x600
	ds_read_b32 v127, v81 offset:0x600
	v_pk_mul_f32 v[250:251], v[70:71], v[166:167] op_sel_hi:[1,0]
	v_pk_fma_f32 v[250:251], v[72:73], v[166:167], v[250:251] op_sel:[0,1,0] op_sel_hi:[1,1,1]
	v_pk_fma_f32 v[250:251], v[74:75], v[168:169], v[250:251] op_sel_hi:[1,0,1]
	v_pk_fma_f32 v[250:251], v[76:77], v[168:169], v[250:251] op_sel:[0,1,0] op_sel_hi:[1,1,1]
	v_pk_mul_f32 v[184:185], v[182:183], v[174:175] op_sel_hi:[1,0]
	v_pk_mul_f32 v[186:187], v[182:183], v[174:175] op_sel:[0,1] op_sel_hi:[1,1]
	v_add_f32_dpp v252, v251, v250 quad_perm:[1,0,3,2] row_mask:0xf bank_mask:0xf bound_ctrl:1
	v_add_f32_dpp v161, v193, v192 quad_perm:[1,0,3,2] row_mask:0xf bank_mask:0xf bound_ctrl:1
	v_pk_mul_f32 v[188:189], v[182:183], v[176:177] op_sel_hi:[1,0]
	v_add_f32_dpp v252, v252, v252 quad_perm:[2,3,0,1] row_mask:0xf bank_mask:0xf bound_ctrl:1
	v_add_f32_dpp v161, v161, v161 quad_perm:[2,3,0,1] row_mask:0xf bank_mask:0xf bound_ctrl:1
	v_pk_mul_f32 v[190:191], v[182:183], v[176:177] op_sel:[0,1] op_sel_hi:[1,1]
	v_add_f32_dpp v252, v252, v252 row_ror:4 row_mask:0xf bank_mask:0xf bound_ctrl:1
	v_add_f32_dpp v161, v161, v161 row_ror:4 row_mask:0xf bank_mask:0xf bound_ctrl:1
	v_pk_fma_f32 v[184:185], v[70:71], v[162:163], v[184:185] op_sel_hi:[1,0,1]
	v_add_f32_dpp v252, v252, v252 row_ror:8 row_mask:0xf bank_mask:0xf bound_ctrl:1
	v_add_f32_dpp v92, v161, v161 row_ror:8 row_mask:0xf bank_mask:0x4 bound_ctrl:1
	v_pk_fma_f32 v[186:187], v[72:73], v[162:163], v[186:187] op_sel:[0,1,0] op_sel_hi:[1,1,1]
	v_mov_b32_dpp v253, v252 quad_perm:[1,0,3,2] row_mask:0xf bank_mask:0xf bound_ctrl:1
	v_pk_fma_f32 v[188:189], v[74:75], v[164:165], v[188:189] op_sel_hi:[1,0,1]
	v_pk_fma_f32 v[190:191], v[76:77], v[164:165], v[190:191] op_sel:[0,1,0] op_sel_hi:[1,1,1]
	v_pk_fma_f32 v[70:71], v[252:253], v[170:171], v[184:185] op_sel_hi:[1,0,1]
	v_pk_fma_f32 v[72:73], v[252:253], v[170:171], v[186:187] op_sel:[0,1,0] op_sel_hi:[1,1,1]
	v_pk_fma_f32 v[74:75], v[252:253], v[172:173], v[188:189] op_sel_hi:[1,0,1]
	v_pk_fma_f32 v[76:77], v[252:253], v[172:173], v[190:191] op_sel:[0,1,0] op_sel_hi:[1,1,1]
	v_pk_mul_f32 v[194:195], v[70:71], v[178:179] op_sel_hi:[1,0]
	v_pk_fma_f32 v[194:195], v[72:73], v[178:179], v[194:195] op_sel:[0,1,0] op_sel_hi:[1,1,1]
	v_pk_fma_f32 v[194:195], v[74:75], v[180:181], v[194:195] op_sel_hi:[1,0,1]
	v_pk_fma_f32 v[194:195], v[76:77], v[180:181], v[194:195] op_sel:[0,1,0] op_sel_hi:[1,1,1]

	s_waitcnt lgkmcnt(0)
	ds_read_b128 v[162:165], v79 offset:0xd00
	ds_read_b128 v[166:169], v79 offset:0x2d00
	ds_read_b128 v[170:173], v79 offset:0x4d00
	ds_read_b128 v[174:177], v79 offset:0x6d00
	ds_read_b128 v[178:181], v79 offset:0x8d00
	ds_read_b32 v182, v80 offset:0x680
	ds_read_b32 v183, v81 offset:0x680
	v_pk_mul_f32 v[250:251], v[70:71], v[86:87] op_sel_hi:[1,0]
	v_pk_fma_f32 v[250:251], v[72:73], v[86:87], v[250:251] op_sel:[0,1,0] op_sel_hi:[1,1,1]
	v_pk_fma_f32 v[250:251], v[74:75], v[88:89], v[250:251] op_sel_hi:[1,0,1]
	v_pk_fma_f32 v[250:251], v[76:77], v[88:89], v[250:251] op_sel:[0,1,0] op_sel_hi:[1,1,1]
	v_pk_mul_f32 v[184:185], v[126:127], v[118:119] op_sel_hi:[1,0]
	v_pk_mul_f32 v[186:187], v[126:127], v[118:119] op_sel:[0,1] op_sel_hi:[1,1]
	v_add_f32_dpp v252, v251, v250 quad_perm:[1,0,3,2] row_mask:0xf bank_mask:0xf bound_ctrl:1
	v_add_f32_dpp v161, v195, v194 quad_perm:[1,0,3,2] row_mask:0xf bank_mask:0xf bound_ctrl:1
	v_pk_mul_f32 v[188:189], v[126:127], v[120:121] op_sel_hi:[1,0]
	v_add_f32_dpp v252, v252, v252 quad_perm:[2,3,0,1] row_mask:0xf bank_mask:0xf bound_ctrl:1
	v_add_f32_dpp v161, v161, v161 quad_perm:[2,3,0,1] row_mask:0xf bank_mask:0xf bound_ctrl:1
	v_pk_mul_f32 v[190:191], v[126:127], v[120:121] op_sel:[0,1] op_sel_hi:[1,1]
	v_add_f32_dpp v252, v252, v252 row_ror:4 row_mask:0xf bank_mask:0xf bound_ctrl:1
	v_add_f32_dpp v161, v161, v161 row_ror:4 row_mask:0xf bank_mask:0xf bound_ctrl:1
	v_pk_fma_f32 v[184:185], v[70:71], v[82:83], v[184:185] op_sel_hi:[1,0,1]
	v_add_f32_dpp v252, v252, v252 row_ror:8 row_mask:0xf bank_mask:0xf bound_ctrl:1
	v_add_f32_dpp v92, v161, v161 row_ror:8 row_mask:0xf bank_mask:0x8 bound_ctrl:1
	v_pk_fma_f32 v[186:187], v[72:73], v[82:83], v[186:187] op_sel:[0,1,0] op_sel_hi:[1,1,1]
	v_mov_b32_dpp v253, v252 quad_perm:[1,0,3,2] row_mask:0xf bank_mask:0xf bound_ctrl:1
	v_pk_fma_f32 v[188:189], v[74:75], v[84:85], v[188:189] op_sel_hi:[1,0,1]
	v_pk_fma_f32 v[190:191], v[76:77], v[84:85], v[190:191] op_sel:[0,1,0] op_sel_hi:[1,1,1]
	v_pk_fma_f32 v[70:71], v[252:253], v[114:115], v[184:185] op_sel_hi:[1,0,1]
	v_pk_fma_f32 v[72:73], v[252:253], v[114:115], v[186:187] op_sel:[0,1,0] op_sel_hi:[1,1,1]
	v_pk_fma_f32 v[74:75], v[252:253], v[116:117], v[188:189] op_sel_hi:[1,0,1]
	v_pk_fma_f32 v[76:77], v[252:253], v[116:117], v[190:191] op_sel:[0,1,0] op_sel_hi:[1,1,1]
	v_pk_mul_f32 v[192:193], v[70:71], v[122:123] op_sel_hi:[1,0]
	v_pk_fma_f32 v[192:193], v[72:73], v[122:123], v[192:193] op_sel:[0,1,0] op_sel_hi:[1,1,1]
	v_pk_fma_f32 v[192:193], v[74:75], v[124:125], v[192:193] op_sel_hi:[1,0,1]
	v_pk_fma_f32 v[192:193], v[76:77], v[124:125], v[192:193] op_sel:[0,1,0] op_sel_hi:[1,1,1]

	s_waitcnt lgkmcnt(0)
	ds_write_b32 v197, v92 offset:1024
	ds_read_b128 v[82:85], v79 offset:0xe00
	ds_read_b128 v[86:89], v79 offset:0x2e00
	ds_read_b128 v[114:117], v79 offset:0x4e00
	ds_read_b128 v[118:121], v79 offset:0x6e00
	ds_read_b128 v[122:125], v79 offset:0x8e00
	ds_read_b32 v126, v80 offset:0x700
	ds_read_b32 v127, v81 offset:0x700
	v_pk_mul_f32 v[250:251], v[70:71], v[166:167] op_sel_hi:[1,0]
	v_pk_fma_f32 v[250:251], v[72:73], v[166:167], v[250:251] op_sel:[0,1,0] op_sel_hi:[1,1,1]
	v_pk_fma_f32 v[250:251], v[74:75], v[168:169], v[250:251] op_sel_hi:[1,0,1]
	v_pk_fma_f32 v[250:251], v[76:77], v[168:169], v[250:251] op_sel:[0,1,0] op_sel_hi:[1,1,1]
	v_pk_mul_f32 v[184:185], v[182:183], v[174:175] op_sel_hi:[1,0]
	v_pk_mul_f32 v[186:187], v[182:183], v[174:175] op_sel:[0,1] op_sel_hi:[1,1]
	v_add_f32_dpp v252, v251, v250 quad_perm:[1,0,3,2] row_mask:0xf bank_mask:0xf bound_ctrl:1
	v_add_f32_dpp v161, v193, v192 quad_perm:[1,0,3,2] row_mask:0xf bank_mask:0xf bound_ctrl:1
	v_pk_mul_f32 v[188:189], v[182:183], v[176:177] op_sel_hi:[1,0]
	v_add_f32_dpp v252, v252, v252 quad_perm:[2,3,0,1] row_mask:0xf bank_mask:0xf bound_ctrl:1
	v_add_f32_dpp v161, v161, v161 quad_perm:[2,3,0,1] row_mask:0xf bank_mask:0xf bound_ctrl:1
	v_pk_mul_f32 v[190:191], v[182:183], v[176:177] op_sel:[0,1] op_sel_hi:[1,1]
	v_add_f32_dpp v252, v252, v252 row_ror:4 row_mask:0xf bank_mask:0xf bound_ctrl:1
	v_add_f32_dpp v161, v161, v161 row_ror:4 row_mask:0xf bank_mask:0xf bound_ctrl:1
	v_pk_fma_f32 v[184:185], v[70:71], v[162:163], v[184:185] op_sel_hi:[1,0,1]
	v_add_f32_dpp v252, v252, v252 row_ror:8 row_mask:0xf bank_mask:0xf bound_ctrl:1
	v_add_f32_dpp v92, v161, v161 row_ror:8 row_mask:0xf bank_mask:0x1 bound_ctrl:1
	v_pk_fma_f32 v[186:187], v[72:73], v[162:163], v[186:187] op_sel:[0,1,0] op_sel_hi:[1,1,1]
	v_mov_b32_dpp v253, v252 quad_perm:[1,0,3,2] row_mask:0xf bank_mask:0xf bound_ctrl:1
	v_pk_fma_f32 v[188:189], v[74:75], v[164:165], v[188:189] op_sel_hi:[1,0,1]
	v_pk_fma_f32 v[190:191], v[76:77], v[164:165], v[190:191] op_sel:[0,1,0] op_sel_hi:[1,1,1]
	v_pk_fma_f32 v[70:71], v[252:253], v[170:171], v[184:185] op_sel_hi:[1,0,1]
	v_pk_fma_f32 v[72:73], v[252:253], v[170:171], v[186:187] op_sel:[0,1,0] op_sel_hi:[1,1,1]
	v_pk_fma_f32 v[74:75], v[252:253], v[172:173], v[188:189] op_sel_hi:[1,0,1]
	v_pk_fma_f32 v[76:77], v[252:253], v[172:173], v[190:191] op_sel:[0,1,0] op_sel_hi:[1,1,1]
	v_pk_mul_f32 v[194:195], v[70:71], v[178:179] op_sel_hi:[1,0]
	v_pk_fma_f32 v[194:195], v[72:73], v[178:179], v[194:195] op_sel:[0,1,0] op_sel_hi:[1,1,1]
	v_pk_fma_f32 v[194:195], v[74:75], v[180:181], v[194:195] op_sel_hi:[1,0,1]
	v_pk_fma_f32 v[194:195], v[76:77], v[180:181], v[194:195] op_sel:[0,1,0] op_sel_hi:[1,1,1]

	s_waitcnt lgkmcnt(0)
	ds_read_b128 v[162:165], v79 offset:0xf00
	ds_read_b128 v[166:169], v79 offset:0x2f00
	ds_read_b128 v[170:173], v79 offset:0x4f00
	ds_read_b128 v[174:177], v79 offset:0x6f00
	ds_read_b128 v[178:181], v79 offset:0x8f00
	ds_read_b32 v182, v80 offset:0x780
	ds_read_b32 v183, v81 offset:0x780
	v_pk_mul_f32 v[250:251], v[70:71], v[86:87] op_sel_hi:[1,0]
	v_pk_fma_f32 v[250:251], v[72:73], v[86:87], v[250:251] op_sel:[0,1,0] op_sel_hi:[1,1,1]
	v_pk_fma_f32 v[250:251], v[74:75], v[88:89], v[250:251] op_sel_hi:[1,0,1]
	v_pk_fma_f32 v[250:251], v[76:77], v[88:89], v[250:251] op_sel:[0,1,0] op_sel_hi:[1,1,1]
	v_pk_mul_f32 v[184:185], v[126:127], v[118:119] op_sel_hi:[1,0]
	v_pk_mul_f32 v[186:187], v[126:127], v[118:119] op_sel:[0,1] op_sel_hi:[1,1]
	v_add_f32_dpp v252, v251, v250 quad_perm:[1,0,3,2] row_mask:0xf bank_mask:0xf bound_ctrl:1
	v_add_f32_dpp v161, v195, v194 quad_perm:[1,0,3,2] row_mask:0xf bank_mask:0xf bound_ctrl:1
	v_pk_mul_f32 v[188:189], v[126:127], v[120:121] op_sel_hi:[1,0]
	v_add_f32_dpp v252, v252, v252 quad_perm:[2,3,0,1] row_mask:0xf bank_mask:0xf bound_ctrl:1
	v_add_f32_dpp v161, v161, v161 quad_perm:[2,3,0,1] row_mask:0xf bank_mask:0xf bound_ctrl:1
	v_pk_mul_f32 v[190:191], v[126:127], v[120:121] op_sel:[0,1] op_sel_hi:[1,1]
	v_add_f32_dpp v252, v252, v252 row_ror:4 row_mask:0xf bank_mask:0xf bound_ctrl:1
	v_add_f32_dpp v161, v161, v161 row_ror:4 row_mask:0xf bank_mask:0xf bound_ctrl:1
	v_pk_fma_f32 v[184:185], v[70:71], v[82:83], v[184:185] op_sel_hi:[1,0,1]
	v_add_f32_dpp v252, v252, v252 row_ror:8 row_mask:0xf bank_mask:0xf bound_ctrl:1
	v_add_f32_dpp v92, v161, v161 row_ror:8 row_mask:0xf bank_mask:0x2 bound_ctrl:1
	v_pk_fma_f32 v[186:187], v[72:73], v[82:83], v[186:187] op_sel:[0,1,0] op_sel_hi:[1,1,1]
	v_mov_b32_dpp v253, v252 quad_perm:[1,0,3,2] row_mask:0xf bank_mask:0xf bound_ctrl:1
	v_pk_fma_f32 v[188:189], v[74:75], v[84:85], v[188:189] op_sel_hi:[1,0,1]
	v_pk_fma_f32 v[190:191], v[76:77], v[84:85], v[190:191] op_sel:[0,1,0] op_sel_hi:[1,1,1]
	v_pk_fma_f32 v[70:71], v[252:253], v[114:115], v[184:185] op_sel_hi:[1,0,1]
	v_pk_fma_f32 v[72:73], v[252:253], v[114:115], v[186:187] op_sel:[0,1,0] op_sel_hi:[1,1,1]
	v_pk_fma_f32 v[74:75], v[252:253], v[116:117], v[188:189] op_sel_hi:[1,0,1]
	v_pk_fma_f32 v[76:77], v[252:253], v[116:117], v[190:191] op_sel:[0,1,0] op_sel_hi:[1,1,1]
	v_pk_mul_f32 v[192:193], v[70:71], v[122:123] op_sel_hi:[1,0]
	v_pk_fma_f32 v[192:193], v[72:73], v[122:123], v[192:193] op_sel:[0,1,0] op_sel_hi:[1,1,1]
	v_pk_fma_f32 v[192:193], v[74:75], v[124:125], v[192:193] op_sel_hi:[1,0,1]
	v_pk_fma_f32 v[192:193], v[76:77], v[124:125], v[192:193] op_sel:[0,1,0] op_sel_hi:[1,1,1]

	s_waitcnt lgkmcnt(0)
	ds_read_b128 v[82:85], v79 offset:0x1000
	ds_read_b128 v[86:89], v79 offset:0x3000
	ds_read_b128 v[114:117], v79 offset:0x5000
	ds_read_b128 v[118:121], v79 offset:0x7000
	ds_read_b128 v[122:125], v79 offset:0x9000
	ds_read_b32 v126, v80 offset:0x800
	ds_read_b32 v127, v81 offset:0x800
	v_pk_mul_f32 v[250:251], v[70:71], v[166:167] op_sel_hi:[1,0]
	v_pk_fma_f32 v[250:251], v[72:73], v[166:167], v[250:251] op_sel:[0,1,0] op_sel_hi:[1,1,1]
	v_pk_fma_f32 v[250:251], v[74:75], v[168:169], v[250:251] op_sel_hi:[1,0,1]
	v_pk_fma_f32 v[250:251], v[76:77], v[168:169], v[250:251] op_sel:[0,1,0] op_sel_hi:[1,1,1]
	v_pk_mul_f32 v[184:185], v[182:183], v[174:175] op_sel_hi:[1,0]
	v_pk_mul_f32 v[186:187], v[182:183], v[174:175] op_sel:[0,1] op_sel_hi:[1,1]
	v_add_f32_dpp v252, v251, v250 quad_perm:[1,0,3,2] row_mask:0xf bank_mask:0xf bound_ctrl:1
	v_add_f32_dpp v161, v193, v192 quad_perm:[1,0,3,2] row_mask:0xf bank_mask:0xf bound_ctrl:1
	v_pk_mul_f32 v[188:189], v[182:183], v[176:177] op_sel_hi:[1,0]
	v_add_f32_dpp v252, v252, v252 quad_perm:[2,3,0,1] row_mask:0xf bank_mask:0xf bound_ctrl:1
	v_add_f32_dpp v161, v161, v161 quad_perm:[2,3,0,1] row_mask:0xf bank_mask:0xf bound_ctrl:1
	v_pk_mul_f32 v[190:191], v[182:183], v[176:177] op_sel:[0,1] op_sel_hi:[1,1]
	v_add_f32_dpp v252, v252, v252 row_ror:4 row_mask:0xf bank_mask:0xf bound_ctrl:1
	v_add_f32_dpp v161, v161, v161 row_ror:4 row_mask:0xf bank_mask:0xf bound_ctrl:1
	v_pk_fma_f32 v[184:185], v[70:71], v[162:163], v[184:185] op_sel_hi:[1,0,1]
	v_add_f32_dpp v252, v252, v252 row_ror:8 row_mask:0xf bank_mask:0xf bound_ctrl:1
	v_add_f32_dpp v92, v161, v161 row_ror:8 row_mask:0xf bank_mask:0x4 bound_ctrl:1
	v_pk_fma_f32 v[186:187], v[72:73], v[162:163], v[186:187] op_sel:[0,1,0] op_sel_hi:[1,1,1]
	v_mov_b32_dpp v253, v252 quad_perm:[1,0,3,2] row_mask:0xf bank_mask:0xf bound_ctrl:1
	v_pk_fma_f32 v[188:189], v[74:75], v[164:165], v[188:189] op_sel_hi:[1,0,1]
	v_pk_fma_f32 v[190:191], v[76:77], v[164:165], v[190:191] op_sel:[0,1,0] op_sel_hi:[1,1,1]
	v_pk_fma_f32 v[70:71], v[252:253], v[170:171], v[184:185] op_sel_hi:[1,0,1]
	v_pk_fma_f32 v[72:73], v[252:253], v[170:171], v[186:187] op_sel:[0,1,0] op_sel_hi:[1,1,1]
	v_pk_fma_f32 v[74:75], v[252:253], v[172:173], v[188:189] op_sel_hi:[1,0,1]
	v_pk_fma_f32 v[76:77], v[252:253], v[172:173], v[190:191] op_sel:[0,1,0] op_sel_hi:[1,1,1]
	v_pk_mul_f32 v[194:195], v[70:71], v[178:179] op_sel_hi:[1,0]
	v_pk_fma_f32 v[194:195], v[72:73], v[178:179], v[194:195] op_sel:[0,1,0] op_sel_hi:[1,1,1]
	v_pk_fma_f32 v[194:195], v[74:75], v[180:181], v[194:195] op_sel_hi:[1,0,1]
	v_pk_fma_f32 v[194:195], v[76:77], v[180:181], v[194:195] op_sel:[0,1,0] op_sel_hi:[1,1,1]

	s_waitcnt lgkmcnt(0)
	ds_read_b128 v[162:165], v79 offset:0x1100
	ds_read_b128 v[166:169], v79 offset:0x3100
	ds_read_b128 v[170:173], v79 offset:0x5100
	ds_read_b128 v[174:177], v79 offset:0x7100
	ds_read_b128 v[178:181], v79 offset:0x9100
	ds_read_b32 v182, v80 offset:0x880
	ds_read_b32 v183, v81 offset:0x880
	v_pk_mul_f32 v[250:251], v[70:71], v[86:87] op_sel_hi:[1,0]
	v_pk_fma_f32 v[250:251], v[72:73], v[86:87], v[250:251] op_sel:[0,1,0] op_sel_hi:[1,1,1]
	v_pk_fma_f32 v[250:251], v[74:75], v[88:89], v[250:251] op_sel_hi:[1,0,1]
	v_pk_fma_f32 v[250:251], v[76:77], v[88:89], v[250:251] op_sel:[0,1,0] op_sel_hi:[1,1,1]
	v_pk_mul_f32 v[184:185], v[126:127], v[118:119] op_sel_hi:[1,0]
	v_pk_mul_f32 v[186:187], v[126:127], v[118:119] op_sel:[0,1] op_sel_hi:[1,1]
	v_add_f32_dpp v252, v251, v250 quad_perm:[1,0,3,2] row_mask:0xf bank_mask:0xf bound_ctrl:1
	v_add_f32_dpp v161, v195, v194 quad_perm:[1,0,3,2] row_mask:0xf bank_mask:0xf bound_ctrl:1
	v_pk_mul_f32 v[188:189], v[126:127], v[120:121] op_sel_hi:[1,0]
	v_add_f32_dpp v252, v252, v252 quad_perm:[2,3,0,1] row_mask:0xf bank_mask:0xf bound_ctrl:1
	v_add_f32_dpp v161, v161, v161 quad_perm:[2,3,0,1] row_mask:0xf bank_mask:0xf bound_ctrl:1
	v_pk_mul_f32 v[190:191], v[126:127], v[120:121] op_sel:[0,1] op_sel_hi:[1,1]
	v_add_f32_dpp v252, v252, v252 row_ror:4 row_mask:0xf bank_mask:0xf bound_ctrl:1
	v_add_f32_dpp v161, v161, v161 row_ror:4 row_mask:0xf bank_mask:0xf bound_ctrl:1
	v_pk_fma_f32 v[184:185], v[70:71], v[82:83], v[184:185] op_sel_hi:[1,0,1]
	v_add_f32_dpp v252, v252, v252 row_ror:8 row_mask:0xf bank_mask:0xf bound_ctrl:1
	v_add_f32_dpp v92, v161, v161 row_ror:8 row_mask:0xf bank_mask:0x8 bound_ctrl:1
	v_pk_fma_f32 v[186:187], v[72:73], v[82:83], v[186:187] op_sel:[0,1,0] op_sel_hi:[1,1,1]
	v_mov_b32_dpp v253, v252 quad_perm:[1,0,3,2] row_mask:0xf bank_mask:0xf bound_ctrl:1
	v_pk_fma_f32 v[188:189], v[74:75], v[84:85], v[188:189] op_sel_hi:[1,0,1]
	v_pk_fma_f32 v[190:191], v[76:77], v[84:85], v[190:191] op_sel:[0,1,0] op_sel_hi:[1,1,1]
	v_pk_fma_f32 v[70:71], v[252:253], v[114:115], v[184:185] op_sel_hi:[1,0,1]
	v_pk_fma_f32 v[72:73], v[252:253], v[114:115], v[186:187] op_sel:[0,1,0] op_sel_hi:[1,1,1]
	v_pk_fma_f32 v[74:75], v[252:253], v[116:117], v[188:189] op_sel_hi:[1,0,1]
	v_pk_fma_f32 v[76:77], v[252:253], v[116:117], v[190:191] op_sel:[0,1,0] op_sel_hi:[1,1,1]
	v_pk_mul_f32 v[192:193], v[70:71], v[122:123] op_sel_hi:[1,0]
	v_pk_fma_f32 v[192:193], v[72:73], v[122:123], v[192:193] op_sel:[0,1,0] op_sel_hi:[1,1,1]
	v_pk_fma_f32 v[192:193], v[74:75], v[124:125], v[192:193] op_sel_hi:[1,0,1]
	v_pk_fma_f32 v[192:193], v[76:77], v[124:125], v[192:193] op_sel:[0,1,0] op_sel_hi:[1,1,1]

	s_nop 0
	ds_write_b32 v197, v92 offset:1536
	s_waitcnt lgkmcnt(0)
	s_nop 0
	ds_read_b128 v[82:85], v79 offset:0x1200
	ds_read_b128 v[86:89], v79 offset:0x3200
	ds_read_b128 v[114:117], v79 offset:0x5200
	ds_read_b128 v[118:121], v79 offset:0x7200
	ds_read_b128 v[122:125], v79 offset:0x9200
	ds_read_b32 v126, v80 offset:0x900
	ds_read_b32 v127, v81 offset:0x900
	v_pk_mul_f32 v[250:251], v[70:71], v[166:167] op_sel_hi:[1,0]
	v_pk_fma_f32 v[250:251], v[72:73], v[166:167], v[250:251] op_sel:[0,1,0] op_sel_hi:[1,1,1]
	v_pk_fma_f32 v[250:251], v[74:75], v[168:169], v[250:251] op_sel_hi:[1,0,1]
	v_pk_fma_f32 v[250:251], v[76:77], v[168:169], v[250:251] op_sel:[0,1,0] op_sel_hi:[1,1,1]
	v_pk_mul_f32 v[184:185], v[182:183], v[174:175] op_sel_hi:[1,0]
	v_pk_mul_f32 v[186:187], v[182:183], v[174:175] op_sel:[0,1] op_sel_hi:[1,1]
	v_add_f32_dpp v252, v251, v250 quad_perm:[1,0,3,2] row_mask:0xf bank_mask:0xf bound_ctrl:1
	v_add_f32_dpp v92, v193, v192 quad_perm:[1,0,3,2] row_mask:0xf bank_mask:0xf bound_ctrl:1
	v_pk_mul_f32 v[188:189], v[182:183], v[176:177] op_sel_hi:[1,0]
	v_add_f32_dpp v252, v252, v252 quad_perm:[2,3,0,1] row_mask:0xf bank_mask:0xf bound_ctrl:1
	v_add_f32_dpp v92, v92, v92 quad_perm:[2,3,0,1] row_mask:0xf bank_mask:0xf bound_ctrl:1
	v_pk_mul_f32 v[190:191], v[182:183], v[176:177] op_sel:[0,1] op_sel_hi:[1,1]
	v_add_f32_dpp v252, v252, v252 row_ror:4 row_mask:0xf bank_mask:0xf bound_ctrl:1
	v_add_f32_dpp v92, v92, v92 row_ror:4 row_mask:0xf bank_mask:0xf bound_ctrl:1
	v_pk_fma_f32 v[184:185], v[70:71], v[162:163], v[184:185] op_sel_hi:[1,0,1]
	v_add_f32_dpp v252, v252, v252 row_ror:8 row_mask:0xf bank_mask:0xf bound_ctrl:1
	v_add_f32_dpp v92, v92, v92 row_ror:8 row_mask:0xf bank_mask:0x1 bound_ctrl:1
	v_pk_fma_f32 v[186:187], v[72:73], v[162:163], v[186:187] op_sel:[0,1,0] op_sel_hi:[1,1,1]
	v_mov_b32_dpp v253, v252 quad_perm:[1,0,3,2] row_mask:0xf bank_mask:0xf bound_ctrl:1
	v_pk_fma_f32 v[188:189], v[74:75], v[164:165], v[188:189] op_sel_hi:[1,0,1]
	v_pk_fma_f32 v[190:191], v[76:77], v[164:165], v[190:191] op_sel:[0,1,0] op_sel_hi:[1,1,1]
	v_pk_fma_f32 v[70:71], v[252:253], v[170:171], v[184:185] op_sel_hi:[1,0,1]
	v_pk_fma_f32 v[72:73], v[252:253], v[170:171], v[186:187] op_sel:[0,1,0] op_sel_hi:[1,1,1]
	v_pk_fma_f32 v[74:75], v[252:253], v[172:173], v[188:189] op_sel_hi:[1,0,1]
	v_pk_fma_f32 v[76:77], v[252:253], v[172:173], v[190:191] op_sel:[0,1,0] op_sel_hi:[1,1,1]
	v_pk_mul_f32 v[194:195], v[70:71], v[178:179] op_sel_hi:[1,0]
	v_pk_fma_f32 v[194:195], v[72:73], v[178:179], v[194:195] op_sel:[0,1,0] op_sel_hi:[1,1,1]
	v_pk_fma_f32 v[194:195], v[74:75], v[180:181], v[194:195] op_sel_hi:[1,0,1]
	v_pk_fma_f32 v[194:195], v[76:77], v[180:181], v[194:195] op_sel:[0,1,0] op_sel_hi:[1,1,1]

	s_waitcnt lgkmcnt(0)
	ds_read_b128 v[162:165], v79 offset:0x1300
	ds_read_b128 v[166:169], v79 offset:0x3300
	ds_read_b128 v[170:173], v79 offset:0x5300
	ds_read_b128 v[174:177], v79 offset:0x7300
	ds_read_b128 v[178:181], v79 offset:0x9300
	ds_read_b32 v182, v80 offset:0x980
	ds_read_b32 v183, v81 offset:0x980
	v_pk_mul_f32 v[250:251], v[70:71], v[86:87] op_sel_hi:[1,0]
	v_pk_fma_f32 v[250:251], v[72:73], v[86:87], v[250:251] op_sel:[0,1,0] op_sel_hi:[1,1,1]
	v_pk_fma_f32 v[250:251], v[74:75], v[88:89], v[250:251] op_sel_hi:[1,0,1]
	v_pk_fma_f32 v[250:251], v[76:77], v[88:89], v[250:251] op_sel:[0,1,0] op_sel_hi:[1,1,1]
	v_pk_mul_f32 v[184:185], v[126:127], v[118:119] op_sel_hi:[1,0]
	v_pk_mul_f32 v[186:187], v[126:127], v[118:119] op_sel:[0,1] op_sel_hi:[1,1]
	v_add_f32_dpp v252, v251, v250 quad_perm:[1,0,3,2] row_mask:0xf bank_mask:0xf bound_ctrl:1
	v_add_f32_dpp v161, v195, v194 quad_perm:[1,0,3,2] row_mask:0xf bank_mask:0xf bound_ctrl:1
	v_pk_mul_f32 v[188:189], v[126:127], v[120:121] op_sel_hi:[1,0]
	v_add_f32_dpp v252, v252, v252 quad_perm:[2,3,0,1] row_mask:0xf bank_mask:0xf bound_ctrl:1
	v_add_f32_dpp v161, v161, v161 quad_perm:[2,3,0,1] row_mask:0xf bank_mask:0xf bound_ctrl:1
	v_pk_mul_f32 v[190:191], v[126:127], v[120:121] op_sel:[0,1] op_sel_hi:[1,1]
	v_add_f32_dpp v252, v252, v252 row_ror:4 row_mask:0xf bank_mask:0xf bound_ctrl:1
	v_add_f32_dpp v161, v161, v161 row_ror:4 row_mask:0xf bank_mask:0xf bound_ctrl:1
	v_pk_fma_f32 v[184:185], v[70:71], v[82:83], v[184:185] op_sel_hi:[1,0,1]
	v_add_f32_dpp v252, v252, v252 row_ror:8 row_mask:0xf bank_mask:0xf bound_ctrl:1
	v_add_f32_dpp v92, v161, v161 row_ror:8 row_mask:0xf bank_mask:0x2 bound_ctrl:1
	v_pk_fma_f32 v[186:187], v[72:73], v[82:83], v[186:187] op_sel:[0,1,0] op_sel_hi:[1,1,1]
	v_mov_b32_dpp v253, v252 quad_perm:[1,0,3,2] row_mask:0xf bank_mask:0xf bound_ctrl:1
	v_pk_fma_f32 v[188:189], v[74:75], v[84:85], v[188:189] op_sel_hi:[1,0,1]
	v_pk_fma_f32 v[190:191], v[76:77], v[84:85], v[190:191] op_sel:[0,1,0] op_sel_hi:[1,1,1]
	v_pk_fma_f32 v[70:71], v[252:253], v[114:115], v[184:185] op_sel_hi:[1,0,1]
	v_pk_fma_f32 v[72:73], v[252:253], v[114:115], v[186:187] op_sel:[0,1,0] op_sel_hi:[1,1,1]
	v_pk_fma_f32 v[74:75], v[252:253], v[116:117], v[188:189] op_sel_hi:[1,0,1]
	v_pk_fma_f32 v[76:77], v[252:253], v[116:117], v[190:191] op_sel:[0,1,0] op_sel_hi:[1,1,1]
	v_pk_mul_f32 v[192:193], v[70:71], v[122:123] op_sel_hi:[1,0]
	v_pk_fma_f32 v[192:193], v[72:73], v[122:123], v[192:193] op_sel:[0,1,0] op_sel_hi:[1,1,1]
	v_pk_fma_f32 v[192:193], v[74:75], v[124:125], v[192:193] op_sel_hi:[1,0,1]
	v_pk_fma_f32 v[192:193], v[76:77], v[124:125], v[192:193] op_sel:[0,1,0] op_sel_hi:[1,1,1]

	s_waitcnt lgkmcnt(0)
	ds_read_b128 v[82:85], v79 offset:0x1400
	ds_read_b128 v[86:89], v79 offset:0x3400
	ds_read_b128 v[114:117], v79 offset:0x5400
	ds_read_b128 v[118:121], v79 offset:0x7400
	ds_read_b128 v[122:125], v79 offset:0x9400
	ds_read_b32 v126, v80 offset:0xa00
	ds_read_b32 v127, v81 offset:0xa00
	v_pk_mul_f32 v[250:251], v[70:71], v[166:167] op_sel_hi:[1,0]
	v_pk_fma_f32 v[250:251], v[72:73], v[166:167], v[250:251] op_sel:[0,1,0] op_sel_hi:[1,1,1]
	v_pk_fma_f32 v[250:251], v[74:75], v[168:169], v[250:251] op_sel_hi:[1,0,1]
	v_pk_fma_f32 v[250:251], v[76:77], v[168:169], v[250:251] op_sel:[0,1,0] op_sel_hi:[1,1,1]
	v_pk_mul_f32 v[184:185], v[182:183], v[174:175] op_sel_hi:[1,0]
	v_pk_mul_f32 v[186:187], v[182:183], v[174:175] op_sel:[0,1] op_sel_hi:[1,1]
	v_add_f32_dpp v252, v251, v250 quad_perm:[1,0,3,2] row_mask:0xf bank_mask:0xf bound_ctrl:1
	v_add_f32_dpp v161, v193, v192 quad_perm:[1,0,3,2] row_mask:0xf bank_mask:0xf bound_ctrl:1
	v_pk_mul_f32 v[188:189], v[182:183], v[176:177] op_sel_hi:[1,0]
	v_add_f32_dpp v252, v252, v252 quad_perm:[2,3,0,1] row_mask:0xf bank_mask:0xf bound_ctrl:1
	v_add_f32_dpp v161, v161, v161 quad_perm:[2,3,0,1] row_mask:0xf bank_mask:0xf bound_ctrl:1
	v_pk_mul_f32 v[190:191], v[182:183], v[176:177] op_sel:[0,1] op_sel_hi:[1,1]
	v_add_f32_dpp v252, v252, v252 row_ror:4 row_mask:0xf bank_mask:0xf bound_ctrl:1
	v_add_f32_dpp v161, v161, v161 row_ror:4 row_mask:0xf bank_mask:0xf bound_ctrl:1
	v_pk_fma_f32 v[184:185], v[70:71], v[162:163], v[184:185] op_sel_hi:[1,0,1]
	v_add_f32_dpp v252, v252, v252 row_ror:8 row_mask:0xf bank_mask:0xf bound_ctrl:1
	v_add_f32_dpp v92, v161, v161 row_ror:8 row_mask:0xf bank_mask:0x4 bound_ctrl:1
	v_pk_fma_f32 v[186:187], v[72:73], v[162:163], v[186:187] op_sel:[0,1,0] op_sel_hi:[1,1,1]
	v_mov_b32_dpp v253, v252 quad_perm:[1,0,3,2] row_mask:0xf bank_mask:0xf bound_ctrl:1
	v_pk_fma_f32 v[188:189], v[74:75], v[164:165], v[188:189] op_sel_hi:[1,0,1]
	v_pk_fma_f32 v[190:191], v[76:77], v[164:165], v[190:191] op_sel:[0,1,0] op_sel_hi:[1,1,1]
	v_pk_fma_f32 v[70:71], v[252:253], v[170:171], v[184:185] op_sel_hi:[1,0,1]
	v_pk_fma_f32 v[72:73], v[252:253], v[170:171], v[186:187] op_sel:[0,1,0] op_sel_hi:[1,1,1]
	v_pk_fma_f32 v[74:75], v[252:253], v[172:173], v[188:189] op_sel_hi:[1,0,1]
	v_pk_fma_f32 v[76:77], v[252:253], v[172:173], v[190:191] op_sel:[0,1,0] op_sel_hi:[1,1,1]
	v_pk_mul_f32 v[194:195], v[70:71], v[178:179] op_sel_hi:[1,0]
	v_pk_fma_f32 v[194:195], v[72:73], v[178:179], v[194:195] op_sel:[0,1,0] op_sel_hi:[1,1,1]
	v_pk_fma_f32 v[194:195], v[74:75], v[180:181], v[194:195] op_sel_hi:[1,0,1]
	v_pk_fma_f32 v[194:195], v[76:77], v[180:181], v[194:195] op_sel:[0,1,0] op_sel_hi:[1,1,1]

	s_waitcnt lgkmcnt(0)
	ds_read_b128 v[162:165], v79 offset:0x1500
	ds_read_b128 v[166:169], v79 offset:0x3500
	ds_read_b128 v[170:173], v79 offset:0x5500
	ds_read_b128 v[174:177], v79 offset:0x7500
	ds_read_b128 v[178:181], v79 offset:0x9500
	ds_read_b32 v182, v80 offset:0xa80
	ds_read_b32 v183, v81 offset:0xa80
	v_pk_mul_f32 v[250:251], v[70:71], v[86:87] op_sel_hi:[1,0]
	v_pk_fma_f32 v[250:251], v[72:73], v[86:87], v[250:251] op_sel:[0,1,0] op_sel_hi:[1,1,1]
	v_pk_fma_f32 v[250:251], v[74:75], v[88:89], v[250:251] op_sel_hi:[1,0,1]
	v_pk_fma_f32 v[250:251], v[76:77], v[88:89], v[250:251] op_sel:[0,1,0] op_sel_hi:[1,1,1]
	v_pk_mul_f32 v[184:185], v[126:127], v[118:119] op_sel_hi:[1,0]
	v_pk_mul_f32 v[186:187], v[126:127], v[118:119] op_sel:[0,1] op_sel_hi:[1,1]
	v_add_f32_dpp v252, v251, v250 quad_perm:[1,0,3,2] row_mask:0xf bank_mask:0xf bound_ctrl:1
	v_add_f32_dpp v161, v195, v194 quad_perm:[1,0,3,2] row_mask:0xf bank_mask:0xf bound_ctrl:1
	v_pk_mul_f32 v[188:189], v[126:127], v[120:121] op_sel_hi:[1,0]
	v_add_f32_dpp v252, v252, v252 quad_perm:[2,3,0,1] row_mask:0xf bank_mask:0xf bound_ctrl:1
	v_add_f32_dpp v161, v161, v161 quad_perm:[2,3,0,1] row_mask:0xf bank_mask:0xf bound_ctrl:1
	v_pk_mul_f32 v[190:191], v[126:127], v[120:121] op_sel:[0,1] op_sel_hi:[1,1]
	v_add_f32_dpp v252, v252, v252 row_ror:4 row_mask:0xf bank_mask:0xf bound_ctrl:1
	v_add_f32_dpp v161, v161, v161 row_ror:4 row_mask:0xf bank_mask:0xf bound_ctrl:1
	v_pk_fma_f32 v[184:185], v[70:71], v[82:83], v[184:185] op_sel_hi:[1,0,1]
	v_add_f32_dpp v252, v252, v252 row_ror:8 row_mask:0xf bank_mask:0xf bound_ctrl:1
	v_add_f32_dpp v92, v161, v161 row_ror:8 row_mask:0xf bank_mask:0x8 bound_ctrl:1
	v_pk_fma_f32 v[186:187], v[72:73], v[82:83], v[186:187] op_sel:[0,1,0] op_sel_hi:[1,1,1]
	v_mov_b32_dpp v253, v252 quad_perm:[1,0,3,2] row_mask:0xf bank_mask:0xf bound_ctrl:1
	v_pk_fma_f32 v[188:189], v[74:75], v[84:85], v[188:189] op_sel_hi:[1,0,1]
	v_pk_fma_f32 v[190:191], v[76:77], v[84:85], v[190:191] op_sel:[0,1,0] op_sel_hi:[1,1,1]
	v_pk_fma_f32 v[70:71], v[252:253], v[114:115], v[184:185] op_sel_hi:[1,0,1]
	v_pk_fma_f32 v[72:73], v[252:253], v[114:115], v[186:187] op_sel:[0,1,0] op_sel_hi:[1,1,1]
	v_pk_fma_f32 v[74:75], v[252:253], v[116:117], v[188:189] op_sel_hi:[1,0,1]
	v_pk_fma_f32 v[76:77], v[252:253], v[116:117], v[190:191] op_sel:[0,1,0] op_sel_hi:[1,1,1]
	v_pk_mul_f32 v[192:193], v[70:71], v[122:123] op_sel_hi:[1,0]
	v_pk_fma_f32 v[192:193], v[72:73], v[122:123], v[192:193] op_sel:[0,1,0] op_sel_hi:[1,1,1]
	v_pk_fma_f32 v[192:193], v[74:75], v[124:125], v[192:193] op_sel_hi:[1,0,1]
	v_pk_fma_f32 v[192:193], v[76:77], v[124:125], v[192:193] op_sel:[0,1,0] op_sel_hi:[1,1,1]

	s_waitcnt lgkmcnt(0)
	ds_write_b32 v197, v92 offset:2048
	ds_read_b128 v[82:85], v79 offset:0x1600
	ds_read_b128 v[86:89], v79 offset:0x3600
	ds_read_b128 v[114:117], v79 offset:0x5600
	ds_read_b128 v[118:121], v79 offset:0x7600
	ds_read_b128 v[122:125], v79 offset:0x9600
	ds_read_b32 v126, v80 offset:0xb00
	ds_read_b32 v127, v81 offset:0xb00
	v_pk_mul_f32 v[250:251], v[70:71], v[166:167] op_sel_hi:[1,0]
	v_pk_fma_f32 v[250:251], v[72:73], v[166:167], v[250:251] op_sel:[0,1,0] op_sel_hi:[1,1,1]
	v_pk_fma_f32 v[250:251], v[74:75], v[168:169], v[250:251] op_sel_hi:[1,0,1]
	v_pk_fma_f32 v[250:251], v[76:77], v[168:169], v[250:251] op_sel:[0,1,0] op_sel_hi:[1,1,1]
	v_pk_mul_f32 v[184:185], v[182:183], v[174:175] op_sel_hi:[1,0]
	v_pk_mul_f32 v[186:187], v[182:183], v[174:175] op_sel:[0,1] op_sel_hi:[1,1]
	v_add_f32_dpp v252, v251, v250 quad_perm:[1,0,3,2] row_mask:0xf bank_mask:0xf bound_ctrl:1
	v_add_f32_dpp v161, v193, v192 quad_perm:[1,0,3,2] row_mask:0xf bank_mask:0xf bound_ctrl:1
	v_pk_mul_f32 v[188:189], v[182:183], v[176:177] op_sel_hi:[1,0]
	v_add_f32_dpp v252, v252, v252 quad_perm:[2,3,0,1] row_mask:0xf bank_mask:0xf bound_ctrl:1
	v_add_f32_dpp v161, v161, v161 quad_perm:[2,3,0,1] row_mask:0xf bank_mask:0xf bound_ctrl:1
	v_pk_mul_f32 v[190:191], v[182:183], v[176:177] op_sel:[0,1] op_sel_hi:[1,1]
	v_add_f32_dpp v252, v252, v252 row_ror:4 row_mask:0xf bank_mask:0xf bound_ctrl:1
	v_add_f32_dpp v161, v161, v161 row_ror:4 row_mask:0xf bank_mask:0xf bound_ctrl:1
	v_pk_fma_f32 v[184:185], v[70:71], v[162:163], v[184:185] op_sel_hi:[1,0,1]
	v_add_f32_dpp v252, v252, v252 row_ror:8 row_mask:0xf bank_mask:0xf bound_ctrl:1
	v_add_f32_dpp v92, v161, v161 row_ror:8 row_mask:0xf bank_mask:0x1 bound_ctrl:1
	v_pk_fma_f32 v[186:187], v[72:73], v[162:163], v[186:187] op_sel:[0,1,0] op_sel_hi:[1,1,1]
	v_mov_b32_dpp v253, v252 quad_perm:[1,0,3,2] row_mask:0xf bank_mask:0xf bound_ctrl:1
	v_pk_fma_f32 v[188:189], v[74:75], v[164:165], v[188:189] op_sel_hi:[1,0,1]
	v_pk_fma_f32 v[190:191], v[76:77], v[164:165], v[190:191] op_sel:[0,1,0] op_sel_hi:[1,1,1]
	v_pk_fma_f32 v[70:71], v[252:253], v[170:171], v[184:185] op_sel_hi:[1,0,1]
	v_pk_fma_f32 v[72:73], v[252:253], v[170:171], v[186:187] op_sel:[0,1,0] op_sel_hi:[1,1,1]
	v_pk_fma_f32 v[74:75], v[252:253], v[172:173], v[188:189] op_sel_hi:[1,0,1]
	v_pk_fma_f32 v[76:77], v[252:253], v[172:173], v[190:191] op_sel:[0,1,0] op_sel_hi:[1,1,1]
	v_pk_mul_f32 v[194:195], v[70:71], v[178:179] op_sel_hi:[1,0]
	v_pk_fma_f32 v[194:195], v[72:73], v[178:179], v[194:195] op_sel:[0,1,0] op_sel_hi:[1,1,1]
	v_pk_fma_f32 v[194:195], v[74:75], v[180:181], v[194:195] op_sel_hi:[1,0,1]
	v_pk_fma_f32 v[194:195], v[76:77], v[180:181], v[194:195] op_sel:[0,1,0] op_sel_hi:[1,1,1]

	s_waitcnt lgkmcnt(0)
	ds_read_b128 v[162:165], v79 offset:0x1700
	ds_read_b128 v[166:169], v79 offset:0x3700
	ds_read_b128 v[170:173], v79 offset:0x5700
	ds_read_b128 v[174:177], v79 offset:0x7700
	ds_read_b128 v[178:181], v79 offset:0x9700
	ds_read_b32 v182, v80 offset:0xb80
	ds_read_b32 v183, v81 offset:0xb80
	v_pk_mul_f32 v[250:251], v[70:71], v[86:87] op_sel_hi:[1,0]
	v_pk_fma_f32 v[250:251], v[72:73], v[86:87], v[250:251] op_sel:[0,1,0] op_sel_hi:[1,1,1]
	v_pk_fma_f32 v[250:251], v[74:75], v[88:89], v[250:251] op_sel_hi:[1,0,1]
	v_pk_fma_f32 v[250:251], v[76:77], v[88:89], v[250:251] op_sel:[0,1,0] op_sel_hi:[1,1,1]
	v_pk_mul_f32 v[184:185], v[126:127], v[118:119] op_sel_hi:[1,0]
	v_pk_mul_f32 v[186:187], v[126:127], v[118:119] op_sel:[0,1] op_sel_hi:[1,1]
	v_add_f32_dpp v252, v251, v250 quad_perm:[1,0,3,2] row_mask:0xf bank_mask:0xf bound_ctrl:1
	v_add_f32_dpp v161, v195, v194 quad_perm:[1,0,3,2] row_mask:0xf bank_mask:0xf bound_ctrl:1
	v_pk_mul_f32 v[188:189], v[126:127], v[120:121] op_sel_hi:[1,0]
	v_add_f32_dpp v252, v252, v252 quad_perm:[2,3,0,1] row_mask:0xf bank_mask:0xf bound_ctrl:1
	v_add_f32_dpp v161, v161, v161 quad_perm:[2,3,0,1] row_mask:0xf bank_mask:0xf bound_ctrl:1
	v_pk_mul_f32 v[190:191], v[126:127], v[120:121] op_sel:[0,1] op_sel_hi:[1,1]
	v_add_f32_dpp v252, v252, v252 row_ror:4 row_mask:0xf bank_mask:0xf bound_ctrl:1
	v_add_f32_dpp v161, v161, v161 row_ror:4 row_mask:0xf bank_mask:0xf bound_ctrl:1
	v_pk_fma_f32 v[184:185], v[70:71], v[82:83], v[184:185] op_sel_hi:[1,0,1]
	v_add_f32_dpp v252, v252, v252 row_ror:8 row_mask:0xf bank_mask:0xf bound_ctrl:1
	v_add_f32_dpp v92, v161, v161 row_ror:8 row_mask:0xf bank_mask:0x2 bound_ctrl:1
	v_pk_fma_f32 v[186:187], v[72:73], v[82:83], v[186:187] op_sel:[0,1,0] op_sel_hi:[1,1,1]
	v_mov_b32_dpp v253, v252 quad_perm:[1,0,3,2] row_mask:0xf bank_mask:0xf bound_ctrl:1
	v_pk_fma_f32 v[188:189], v[74:75], v[84:85], v[188:189] op_sel_hi:[1,0,1]
	v_pk_fma_f32 v[190:191], v[76:77], v[84:85], v[190:191] op_sel:[0,1,0] op_sel_hi:[1,1,1]
	v_pk_fma_f32 v[70:71], v[252:253], v[114:115], v[184:185] op_sel_hi:[1,0,1]
	v_pk_fma_f32 v[72:73], v[252:253], v[114:115], v[186:187] op_sel:[0,1,0] op_sel_hi:[1,1,1]
	v_pk_fma_f32 v[74:75], v[252:253], v[116:117], v[188:189] op_sel_hi:[1,0,1]
	v_pk_fma_f32 v[76:77], v[252:253], v[116:117], v[190:191] op_sel:[0,1,0] op_sel_hi:[1,1,1]
	v_pk_mul_f32 v[192:193], v[70:71], v[122:123] op_sel_hi:[1,0]
	v_pk_fma_f32 v[192:193], v[72:73], v[122:123], v[192:193] op_sel:[0,1,0] op_sel_hi:[1,1,1]
	v_pk_fma_f32 v[192:193], v[74:75], v[124:125], v[192:193] op_sel_hi:[1,0,1]
	v_pk_fma_f32 v[192:193], v[76:77], v[124:125], v[192:193] op_sel:[0,1,0] op_sel_hi:[1,1,1]

	s_waitcnt lgkmcnt(0)
	ds_read_b128 v[82:85], v79 offset:0x1800
	ds_read_b128 v[86:89], v79 offset:0x3800
	ds_read_b128 v[114:117], v79 offset:0x5800
	ds_read_b128 v[118:121], v79 offset:0x7800
	ds_read_b128 v[122:125], v79 offset:0x9800
	ds_read_b32 v126, v80 offset:0xc00
	ds_read_b32 v127, v81 offset:0xc00
	v_pk_mul_f32 v[250:251], v[70:71], v[166:167] op_sel_hi:[1,0]
	v_pk_fma_f32 v[250:251], v[72:73], v[166:167], v[250:251] op_sel:[0,1,0] op_sel_hi:[1,1,1]
	v_pk_fma_f32 v[250:251], v[74:75], v[168:169], v[250:251] op_sel_hi:[1,0,1]
	v_pk_fma_f32 v[250:251], v[76:77], v[168:169], v[250:251] op_sel:[0,1,0] op_sel_hi:[1,1,1]
	v_pk_mul_f32 v[184:185], v[182:183], v[174:175] op_sel_hi:[1,0]
	v_pk_mul_f32 v[186:187], v[182:183], v[174:175] op_sel:[0,1] op_sel_hi:[1,1]
	v_add_f32_dpp v252, v251, v250 quad_perm:[1,0,3,2] row_mask:0xf bank_mask:0xf bound_ctrl:1
	v_add_f32_dpp v161, v193, v192 quad_perm:[1,0,3,2] row_mask:0xf bank_mask:0xf bound_ctrl:1
	v_pk_mul_f32 v[188:189], v[182:183], v[176:177] op_sel_hi:[1,0]
	v_add_f32_dpp v252, v252, v252 quad_perm:[2,3,0,1] row_mask:0xf bank_mask:0xf bound_ctrl:1
	v_add_f32_dpp v161, v161, v161 quad_perm:[2,3,0,1] row_mask:0xf bank_mask:0xf bound_ctrl:1
	v_pk_mul_f32 v[190:191], v[182:183], v[176:177] op_sel:[0,1] op_sel_hi:[1,1]
	v_add_f32_dpp v252, v252, v252 row_ror:4 row_mask:0xf bank_mask:0xf bound_ctrl:1
	v_add_f32_dpp v161, v161, v161 row_ror:4 row_mask:0xf bank_mask:0xf bound_ctrl:1
	v_pk_fma_f32 v[184:185], v[70:71], v[162:163], v[184:185] op_sel_hi:[1,0,1]
	v_add_f32_dpp v252, v252, v252 row_ror:8 row_mask:0xf bank_mask:0xf bound_ctrl:1
	v_add_f32_dpp v92, v161, v161 row_ror:8 row_mask:0xf bank_mask:0x4 bound_ctrl:1
	v_pk_fma_f32 v[186:187], v[72:73], v[162:163], v[186:187] op_sel:[0,1,0] op_sel_hi:[1,1,1]
	v_mov_b32_dpp v253, v252 quad_perm:[1,0,3,2] row_mask:0xf bank_mask:0xf bound_ctrl:1
	v_pk_fma_f32 v[188:189], v[74:75], v[164:165], v[188:189] op_sel_hi:[1,0,1]
	v_pk_fma_f32 v[190:191], v[76:77], v[164:165], v[190:191] op_sel:[0,1,0] op_sel_hi:[1,1,1]
	v_pk_fma_f32 v[70:71], v[252:253], v[170:171], v[184:185] op_sel_hi:[1,0,1]
	v_pk_fma_f32 v[72:73], v[252:253], v[170:171], v[186:187] op_sel:[0,1,0] op_sel_hi:[1,1,1]
	v_pk_fma_f32 v[74:75], v[252:253], v[172:173], v[188:189] op_sel_hi:[1,0,1]
	v_pk_fma_f32 v[76:77], v[252:253], v[172:173], v[190:191] op_sel:[0,1,0] op_sel_hi:[1,1,1]
	v_pk_mul_f32 v[194:195], v[70:71], v[178:179] op_sel_hi:[1,0]
	v_pk_fma_f32 v[194:195], v[72:73], v[178:179], v[194:195] op_sel:[0,1,0] op_sel_hi:[1,1,1]
	v_pk_fma_f32 v[194:195], v[74:75], v[180:181], v[194:195] op_sel_hi:[1,0,1]
	v_pk_fma_f32 v[194:195], v[76:77], v[180:181], v[194:195] op_sel:[0,1,0] op_sel_hi:[1,1,1]

	s_waitcnt lgkmcnt(0)
	ds_read_b128 v[162:165], v79 offset:0x1900
	ds_read_b128 v[166:169], v79 offset:0x3900
	ds_read_b128 v[170:173], v79 offset:0x5900
	ds_read_b128 v[174:177], v79 offset:0x7900
	ds_read_b128 v[178:181], v79 offset:0x9900
	ds_read_b32 v182, v80 offset:0xc80
	ds_read_b32 v183, v81 offset:0xc80
	v_pk_mul_f32 v[250:251], v[70:71], v[86:87] op_sel_hi:[1,0]
	v_pk_fma_f32 v[250:251], v[72:73], v[86:87], v[250:251] op_sel:[0,1,0] op_sel_hi:[1,1,1]
	v_pk_fma_f32 v[250:251], v[74:75], v[88:89], v[250:251] op_sel_hi:[1,0,1]
	v_pk_fma_f32 v[250:251], v[76:77], v[88:89], v[250:251] op_sel:[0,1,0] op_sel_hi:[1,1,1]
	v_pk_mul_f32 v[184:185], v[126:127], v[118:119] op_sel_hi:[1,0]
	v_pk_mul_f32 v[186:187], v[126:127], v[118:119] op_sel:[0,1] op_sel_hi:[1,1]
	v_add_f32_dpp v252, v251, v250 quad_perm:[1,0,3,2] row_mask:0xf bank_mask:0xf bound_ctrl:1
	v_add_f32_dpp v161, v195, v194 quad_perm:[1,0,3,2] row_mask:0xf bank_mask:0xf bound_ctrl:1
	v_pk_mul_f32 v[188:189], v[126:127], v[120:121] op_sel_hi:[1,0]
	v_add_f32_dpp v252, v252, v252 quad_perm:[2,3,0,1] row_mask:0xf bank_mask:0xf bound_ctrl:1
	v_add_f32_dpp v161, v161, v161 quad_perm:[2,3,0,1] row_mask:0xf bank_mask:0xf bound_ctrl:1
	v_pk_mul_f32 v[190:191], v[126:127], v[120:121] op_sel:[0,1] op_sel_hi:[1,1]
	v_add_f32_dpp v252, v252, v252 row_ror:4 row_mask:0xf bank_mask:0xf bound_ctrl:1
	v_add_f32_dpp v161, v161, v161 row_ror:4 row_mask:0xf bank_mask:0xf bound_ctrl:1
	v_pk_fma_f32 v[184:185], v[70:71], v[82:83], v[184:185] op_sel_hi:[1,0,1]
	v_add_f32_dpp v252, v252, v252 row_ror:8 row_mask:0xf bank_mask:0xf bound_ctrl:1
	v_add_f32_dpp v92, v161, v161 row_ror:8 row_mask:0xf bank_mask:0x8 bound_ctrl:1
	v_pk_fma_f32 v[186:187], v[72:73], v[82:83], v[186:187] op_sel:[0,1,0] op_sel_hi:[1,1,1]
	v_mov_b32_dpp v253, v252 quad_perm:[1,0,3,2] row_mask:0xf bank_mask:0xf bound_ctrl:1
	v_pk_fma_f32 v[188:189], v[74:75], v[84:85], v[188:189] op_sel_hi:[1,0,1]
	v_pk_fma_f32 v[190:191], v[76:77], v[84:85], v[190:191] op_sel:[0,1,0] op_sel_hi:[1,1,1]
	v_pk_fma_f32 v[70:71], v[252:253], v[114:115], v[184:185] op_sel_hi:[1,0,1]
	v_pk_fma_f32 v[72:73], v[252:253], v[114:115], v[186:187] op_sel:[0,1,0] op_sel_hi:[1,1,1]
	v_pk_fma_f32 v[74:75], v[252:253], v[116:117], v[188:189] op_sel_hi:[1,0,1]
	v_pk_fma_f32 v[76:77], v[252:253], v[116:117], v[190:191] op_sel:[0,1,0] op_sel_hi:[1,1,1]
	v_pk_mul_f32 v[192:193], v[70:71], v[122:123] op_sel_hi:[1,0]
	v_pk_fma_f32 v[192:193], v[72:73], v[122:123], v[192:193] op_sel:[0,1,0] op_sel_hi:[1,1,1]
	v_pk_fma_f32 v[192:193], v[74:75], v[124:125], v[192:193] op_sel_hi:[1,0,1]
	v_pk_fma_f32 v[192:193], v[76:77], v[124:125], v[192:193] op_sel:[0,1,0] op_sel_hi:[1,1,1]

	s_nop 0
	ds_write_b32 v197, v92 offset:2560
	s_waitcnt lgkmcnt(0)
	s_nop 0
	ds_read_b128 v[82:85], v79 offset:0x1a00
	ds_read_b128 v[86:89], v79 offset:0x3a00
	ds_read_b128 v[114:117], v79 offset:0x5a00
	ds_read_b128 v[118:121], v79 offset:0x7a00
	ds_read_b128 v[122:125], v79 offset:0x9a00
	ds_read_b32 v126, v80 offset:0xd00
	ds_read_b32 v127, v81 offset:0xd00
	v_pk_mul_f32 v[250:251], v[70:71], v[166:167] op_sel_hi:[1,0]
	v_pk_fma_f32 v[250:251], v[72:73], v[166:167], v[250:251] op_sel:[0,1,0] op_sel_hi:[1,1,1]
	v_pk_fma_f32 v[250:251], v[74:75], v[168:169], v[250:251] op_sel_hi:[1,0,1]
	v_pk_fma_f32 v[250:251], v[76:77], v[168:169], v[250:251] op_sel:[0,1,0] op_sel_hi:[1,1,1]
	v_pk_mul_f32 v[184:185], v[182:183], v[174:175] op_sel_hi:[1,0]
	v_pk_mul_f32 v[186:187], v[182:183], v[174:175] op_sel:[0,1] op_sel_hi:[1,1]
	v_add_f32_dpp v252, v251, v250 quad_perm:[1,0,3,2] row_mask:0xf bank_mask:0xf bound_ctrl:1
	v_add_f32_dpp v92, v193, v192 quad_perm:[1,0,3,2] row_mask:0xf bank_mask:0xf bound_ctrl:1
	v_pk_mul_f32 v[188:189], v[182:183], v[176:177] op_sel_hi:[1,0]
	v_add_f32_dpp v252, v252, v252 quad_perm:[2,3,0,1] row_mask:0xf bank_mask:0xf bound_ctrl:1
	v_add_f32_dpp v92, v92, v92 quad_perm:[2,3,0,1] row_mask:0xf bank_mask:0xf bound_ctrl:1
	v_pk_mul_f32 v[190:191], v[182:183], v[176:177] op_sel:[0,1] op_sel_hi:[1,1]
	v_add_f32_dpp v252, v252, v252 row_ror:4 row_mask:0xf bank_mask:0xf bound_ctrl:1
	v_add_f32_dpp v92, v92, v92 row_ror:4 row_mask:0xf bank_mask:0xf bound_ctrl:1
	v_pk_fma_f32 v[184:185], v[70:71], v[162:163], v[184:185] op_sel_hi:[1,0,1]
	v_add_f32_dpp v252, v252, v252 row_ror:8 row_mask:0xf bank_mask:0xf bound_ctrl:1
	v_add_f32_dpp v92, v92, v92 row_ror:8 row_mask:0xf bank_mask:0x1 bound_ctrl:1
	v_pk_fma_f32 v[186:187], v[72:73], v[162:163], v[186:187] op_sel:[0,1,0] op_sel_hi:[1,1,1]
	v_mov_b32_dpp v253, v252 quad_perm:[1,0,3,2] row_mask:0xf bank_mask:0xf bound_ctrl:1
	v_pk_fma_f32 v[188:189], v[74:75], v[164:165], v[188:189] op_sel_hi:[1,0,1]
	v_pk_fma_f32 v[190:191], v[76:77], v[164:165], v[190:191] op_sel:[0,1,0] op_sel_hi:[1,1,1]
	v_pk_fma_f32 v[70:71], v[252:253], v[170:171], v[184:185] op_sel_hi:[1,0,1]
	v_pk_fma_f32 v[72:73], v[252:253], v[170:171], v[186:187] op_sel:[0,1,0] op_sel_hi:[1,1,1]
	v_pk_fma_f32 v[74:75], v[252:253], v[172:173], v[188:189] op_sel_hi:[1,0,1]
	v_pk_fma_f32 v[76:77], v[252:253], v[172:173], v[190:191] op_sel:[0,1,0] op_sel_hi:[1,1,1]
	v_pk_mul_f32 v[194:195], v[70:71], v[178:179] op_sel_hi:[1,0]
	v_pk_fma_f32 v[194:195], v[72:73], v[178:179], v[194:195] op_sel:[0,1,0] op_sel_hi:[1,1,1]
	v_pk_fma_f32 v[194:195], v[74:75], v[180:181], v[194:195] op_sel_hi:[1,0,1]
	v_pk_fma_f32 v[194:195], v[76:77], v[180:181], v[194:195] op_sel:[0,1,0] op_sel_hi:[1,1,1]

	s_waitcnt lgkmcnt(0)
	ds_read_b128 v[162:165], v79 offset:0x1b00
	ds_read_b128 v[166:169], v79 offset:0x3b00
	ds_read_b128 v[170:173], v79 offset:0x5b00
	ds_read_b128 v[174:177], v79 offset:0x7b00
	ds_read_b128 v[178:181], v79 offset:0x9b00
	ds_read_b32 v182, v80 offset:0xd80
	ds_read_b32 v183, v81 offset:0xd80
	v_pk_mul_f32 v[250:251], v[70:71], v[86:87] op_sel_hi:[1,0]
	v_pk_fma_f32 v[250:251], v[72:73], v[86:87], v[250:251] op_sel:[0,1,0] op_sel_hi:[1,1,1]
	v_pk_fma_f32 v[250:251], v[74:75], v[88:89], v[250:251] op_sel_hi:[1,0,1]
	v_pk_fma_f32 v[250:251], v[76:77], v[88:89], v[250:251] op_sel:[0,1,0] op_sel_hi:[1,1,1]
	v_pk_mul_f32 v[184:185], v[126:127], v[118:119] op_sel_hi:[1,0]
	v_pk_mul_f32 v[186:187], v[126:127], v[118:119] op_sel:[0,1] op_sel_hi:[1,1]
	v_add_f32_dpp v252, v251, v250 quad_perm:[1,0,3,2] row_mask:0xf bank_mask:0xf bound_ctrl:1
	v_add_f32_dpp v161, v195, v194 quad_perm:[1,0,3,2] row_mask:0xf bank_mask:0xf bound_ctrl:1
	v_pk_mul_f32 v[188:189], v[126:127], v[120:121] op_sel_hi:[1,0]
	v_add_f32_dpp v252, v252, v252 quad_perm:[2,3,0,1] row_mask:0xf bank_mask:0xf bound_ctrl:1
	v_add_f32_dpp v161, v161, v161 quad_perm:[2,3,0,1] row_mask:0xf bank_mask:0xf bound_ctrl:1
	v_pk_mul_f32 v[190:191], v[126:127], v[120:121] op_sel:[0,1] op_sel_hi:[1,1]
	v_add_f32_dpp v252, v252, v252 row_ror:4 row_mask:0xf bank_mask:0xf bound_ctrl:1
	v_add_f32_dpp v161, v161, v161 row_ror:4 row_mask:0xf bank_mask:0xf bound_ctrl:1
	v_pk_fma_f32 v[184:185], v[70:71], v[82:83], v[184:185] op_sel_hi:[1,0,1]
	v_add_f32_dpp v252, v252, v252 row_ror:8 row_mask:0xf bank_mask:0xf bound_ctrl:1
	v_add_f32_dpp v92, v161, v161 row_ror:8 row_mask:0xf bank_mask:0x2 bound_ctrl:1
	v_pk_fma_f32 v[186:187], v[72:73], v[82:83], v[186:187] op_sel:[0,1,0] op_sel_hi:[1,1,1]
	v_mov_b32_dpp v253, v252 quad_perm:[1,0,3,2] row_mask:0xf bank_mask:0xf bound_ctrl:1
	v_pk_fma_f32 v[188:189], v[74:75], v[84:85], v[188:189] op_sel_hi:[1,0,1]
	v_pk_fma_f32 v[190:191], v[76:77], v[84:85], v[190:191] op_sel:[0,1,0] op_sel_hi:[1,1,1]
	v_pk_fma_f32 v[70:71], v[252:253], v[114:115], v[184:185] op_sel_hi:[1,0,1]
	v_pk_fma_f32 v[72:73], v[252:253], v[114:115], v[186:187] op_sel:[0,1,0] op_sel_hi:[1,1,1]
	v_pk_fma_f32 v[74:75], v[252:253], v[116:117], v[188:189] op_sel_hi:[1,0,1]
	v_pk_fma_f32 v[76:77], v[252:253], v[116:117], v[190:191] op_sel:[0,1,0] op_sel_hi:[1,1,1]
	v_pk_mul_f32 v[192:193], v[70:71], v[122:123] op_sel_hi:[1,0]
	v_pk_fma_f32 v[192:193], v[72:73], v[122:123], v[192:193] op_sel:[0,1,0] op_sel_hi:[1,1,1]
	v_pk_fma_f32 v[192:193], v[74:75], v[124:125], v[192:193] op_sel_hi:[1,0,1]
	v_pk_fma_f32 v[192:193], v[76:77], v[124:125], v[192:193] op_sel:[0,1,0] op_sel_hi:[1,1,1]

	s_waitcnt lgkmcnt(0)
	ds_read_b128 v[82:85], v79 offset:0x1c00
	ds_read_b128 v[86:89], v79 offset:0x3c00
	ds_read_b128 v[114:117], v79 offset:0x5c00
	ds_read_b128 v[118:121], v79 offset:0x7c00
	ds_read_b128 v[122:125], v79 offset:0x9c00
	ds_read_b32 v126, v80 offset:0xe00
	ds_read_b32 v127, v81 offset:0xe00
	v_pk_mul_f32 v[250:251], v[70:71], v[166:167] op_sel_hi:[1,0]
	v_pk_fma_f32 v[250:251], v[72:73], v[166:167], v[250:251] op_sel:[0,1,0] op_sel_hi:[1,1,1]
	v_pk_fma_f32 v[250:251], v[74:75], v[168:169], v[250:251] op_sel_hi:[1,0,1]
	v_pk_fma_f32 v[250:251], v[76:77], v[168:169], v[250:251] op_sel:[0,1,0] op_sel_hi:[1,1,1]
	v_pk_mul_f32 v[184:185], v[182:183], v[174:175] op_sel_hi:[1,0]
	v_pk_mul_f32 v[186:187], v[182:183], v[174:175] op_sel:[0,1] op_sel_hi:[1,1]
	v_add_f32_dpp v252, v251, v250 quad_perm:[1,0,3,2] row_mask:0xf bank_mask:0xf bound_ctrl:1
	v_add_f32_dpp v161, v193, v192 quad_perm:[1,0,3,2] row_mask:0xf bank_mask:0xf bound_ctrl:1
	v_pk_mul_f32 v[188:189], v[182:183], v[176:177] op_sel_hi:[1,0]
	v_add_f32_dpp v252, v252, v252 quad_perm:[2,3,0,1] row_mask:0xf bank_mask:0xf bound_ctrl:1
	v_add_f32_dpp v161, v161, v161 quad_perm:[2,3,0,1] row_mask:0xf bank_mask:0xf bound_ctrl:1
	v_pk_mul_f32 v[190:191], v[182:183], v[176:177] op_sel:[0,1] op_sel_hi:[1,1]
	v_add_f32_dpp v252, v252, v252 row_ror:4 row_mask:0xf bank_mask:0xf bound_ctrl:1
	v_add_f32_dpp v161, v161, v161 row_ror:4 row_mask:0xf bank_mask:0xf bound_ctrl:1
	v_pk_fma_f32 v[184:185], v[70:71], v[162:163], v[184:185] op_sel_hi:[1,0,1]
	v_add_f32_dpp v252, v252, v252 row_ror:8 row_mask:0xf bank_mask:0xf bound_ctrl:1
	v_add_f32_dpp v92, v161, v161 row_ror:8 row_mask:0xf bank_mask:0x4 bound_ctrl:1
	v_pk_fma_f32 v[186:187], v[72:73], v[162:163], v[186:187] op_sel:[0,1,0] op_sel_hi:[1,1,1]
	v_mov_b32_dpp v253, v252 quad_perm:[1,0,3,2] row_mask:0xf bank_mask:0xf bound_ctrl:1
	v_pk_fma_f32 v[188:189], v[74:75], v[164:165], v[188:189] op_sel_hi:[1,0,1]
	v_pk_fma_f32 v[190:191], v[76:77], v[164:165], v[190:191] op_sel:[0,1,0] op_sel_hi:[1,1,1]
	v_pk_fma_f32 v[70:71], v[252:253], v[170:171], v[184:185] op_sel_hi:[1,0,1]
	v_pk_fma_f32 v[72:73], v[252:253], v[170:171], v[186:187] op_sel:[0,1,0] op_sel_hi:[1,1,1]
	v_pk_fma_f32 v[74:75], v[252:253], v[172:173], v[188:189] op_sel_hi:[1,0,1]
	v_pk_fma_f32 v[76:77], v[252:253], v[172:173], v[190:191] op_sel:[0,1,0] op_sel_hi:[1,1,1]
	v_pk_mul_f32 v[194:195], v[70:71], v[178:179] op_sel_hi:[1,0]
	v_pk_fma_f32 v[194:195], v[72:73], v[178:179], v[194:195] op_sel:[0,1,0] op_sel_hi:[1,1,1]
	v_pk_fma_f32 v[194:195], v[74:75], v[180:181], v[194:195] op_sel_hi:[1,0,1]
	v_pk_fma_f32 v[194:195], v[76:77], v[180:181], v[194:195] op_sel:[0,1,0] op_sel_hi:[1,1,1]

	s_waitcnt lgkmcnt(0)
	ds_read_b128 v[162:165], v79 offset:0x1d00
	ds_read_b128 v[166:169], v79 offset:0x3d00
	ds_read_b128 v[170:173], v79 offset:0x5d00
	ds_read_b128 v[174:177], v79 offset:0x7d00
	ds_read_b128 v[178:181], v79 offset:0x9d00
	ds_read_b32 v182, v80 offset:0xe80
	ds_read_b32 v183, v81 offset:0xe80
	v_pk_mul_f32 v[250:251], v[70:71], v[86:87] op_sel_hi:[1,0]
	v_pk_fma_f32 v[250:251], v[72:73], v[86:87], v[250:251] op_sel:[0,1,0] op_sel_hi:[1,1,1]
	v_pk_fma_f32 v[250:251], v[74:75], v[88:89], v[250:251] op_sel_hi:[1,0,1]
	v_pk_fma_f32 v[250:251], v[76:77], v[88:89], v[250:251] op_sel:[0,1,0] op_sel_hi:[1,1,1]
	v_pk_mul_f32 v[184:185], v[126:127], v[118:119] op_sel_hi:[1,0]
	v_pk_mul_f32 v[186:187], v[126:127], v[118:119] op_sel:[0,1] op_sel_hi:[1,1]
	v_add_f32_dpp v252, v251, v250 quad_perm:[1,0,3,2] row_mask:0xf bank_mask:0xf bound_ctrl:1
	v_add_f32_dpp v161, v195, v194 quad_perm:[1,0,3,2] row_mask:0xf bank_mask:0xf bound_ctrl:1
	v_pk_mul_f32 v[188:189], v[126:127], v[120:121] op_sel_hi:[1,0]
	v_add_f32_dpp v252, v252, v252 quad_perm:[2,3,0,1] row_mask:0xf bank_mask:0xf bound_ctrl:1
	v_add_f32_dpp v161, v161, v161 quad_perm:[2,3,0,1] row_mask:0xf bank_mask:0xf bound_ctrl:1
	v_pk_mul_f32 v[190:191], v[126:127], v[120:121] op_sel:[0,1] op_sel_hi:[1,1]
	v_add_f32_dpp v252, v252, v252 row_ror:4 row_mask:0xf bank_mask:0xf bound_ctrl:1
	v_add_f32_dpp v161, v161, v161 row_ror:4 row_mask:0xf bank_mask:0xf bound_ctrl:1
	v_pk_fma_f32 v[184:185], v[70:71], v[82:83], v[184:185] op_sel_hi:[1,0,1]
	v_add_f32_dpp v252, v252, v252 row_ror:8 row_mask:0xf bank_mask:0xf bound_ctrl:1
	v_add_f32_dpp v92, v161, v161 row_ror:8 row_mask:0xf bank_mask:0x8 bound_ctrl:1
	v_pk_fma_f32 v[186:187], v[72:73], v[82:83], v[186:187] op_sel:[0,1,0] op_sel_hi:[1,1,1]
	v_mov_b32_dpp v253, v252 quad_perm:[1,0,3,2] row_mask:0xf bank_mask:0xf bound_ctrl:1
	v_pk_fma_f32 v[188:189], v[74:75], v[84:85], v[188:189] op_sel_hi:[1,0,1]
	v_pk_fma_f32 v[190:191], v[76:77], v[84:85], v[190:191] op_sel:[0,1,0] op_sel_hi:[1,1,1]
	v_pk_fma_f32 v[70:71], v[252:253], v[114:115], v[184:185] op_sel_hi:[1,0,1]
	v_pk_fma_f32 v[72:73], v[252:253], v[114:115], v[186:187] op_sel:[0,1,0] op_sel_hi:[1,1,1]
	v_pk_fma_f32 v[74:75], v[252:253], v[116:117], v[188:189] op_sel_hi:[1,0,1]
	v_pk_fma_f32 v[76:77], v[252:253], v[116:117], v[190:191] op_sel:[0,1,0] op_sel_hi:[1,1,1]
	v_pk_mul_f32 v[192:193], v[70:71], v[122:123] op_sel_hi:[1,0]
	v_pk_fma_f32 v[192:193], v[72:73], v[122:123], v[192:193] op_sel:[0,1,0] op_sel_hi:[1,1,1]
	v_pk_fma_f32 v[192:193], v[74:75], v[124:125], v[192:193] op_sel_hi:[1,0,1]
	v_pk_fma_f32 v[192:193], v[76:77], v[124:125], v[192:193] op_sel:[0,1,0] op_sel_hi:[1,1,1]

	s_waitcnt lgkmcnt(0)
	ds_write_b32 v197, v92 offset:3072
	ds_read_b128 v[82:85], v79 offset:0x1e00
	ds_read_b128 v[86:89], v79 offset:0x3e00
	ds_read_b128 v[114:117], v79 offset:0x5e00
	ds_read_b128 v[118:121], v79 offset:0x7e00
	ds_read_b128 v[122:125], v79 offset:0x9e00
	ds_read_b32 v126, v80 offset:0xf00
	ds_read_b32 v127, v81 offset:0xf00
	v_pk_mul_f32 v[250:251], v[70:71], v[166:167] op_sel_hi:[1,0]
	v_pk_fma_f32 v[250:251], v[72:73], v[166:167], v[250:251] op_sel:[0,1,0] op_sel_hi:[1,1,1]
	v_pk_fma_f32 v[250:251], v[74:75], v[168:169], v[250:251] op_sel_hi:[1,0,1]
	v_pk_fma_f32 v[250:251], v[76:77], v[168:169], v[250:251] op_sel:[0,1,0] op_sel_hi:[1,1,1]
	v_pk_mul_f32 v[184:185], v[182:183], v[174:175] op_sel_hi:[1,0]
	v_pk_mul_f32 v[186:187], v[182:183], v[174:175] op_sel:[0,1] op_sel_hi:[1,1]
	v_add_f32_dpp v252, v251, v250 quad_perm:[1,0,3,2] row_mask:0xf bank_mask:0xf bound_ctrl:1
	v_add_f32_dpp v161, v193, v192 quad_perm:[1,0,3,2] row_mask:0xf bank_mask:0xf bound_ctrl:1
	v_pk_mul_f32 v[188:189], v[182:183], v[176:177] op_sel_hi:[1,0]
	v_add_f32_dpp v252, v252, v252 quad_perm:[2,3,0,1] row_mask:0xf bank_mask:0xf bound_ctrl:1
	v_add_f32_dpp v161, v161, v161 quad_perm:[2,3,0,1] row_mask:0xf bank_mask:0xf bound_ctrl:1
	v_pk_mul_f32 v[190:191], v[182:183], v[176:177] op_sel:[0,1] op_sel_hi:[1,1]
	v_add_f32_dpp v252, v252, v252 row_ror:4 row_mask:0xf bank_mask:0xf bound_ctrl:1
	v_add_f32_dpp v161, v161, v161 row_ror:4 row_mask:0xf bank_mask:0xf bound_ctrl:1
	v_pk_fma_f32 v[184:185], v[70:71], v[162:163], v[184:185] op_sel_hi:[1,0,1]
	v_add_f32_dpp v252, v252, v252 row_ror:8 row_mask:0xf bank_mask:0xf bound_ctrl:1
	v_add_f32_dpp v92, v161, v161 row_ror:8 row_mask:0xf bank_mask:0x1 bound_ctrl:1
	v_pk_fma_f32 v[186:187], v[72:73], v[162:163], v[186:187] op_sel:[0,1,0] op_sel_hi:[1,1,1]
	v_mov_b32_dpp v253, v252 quad_perm:[1,0,3,2] row_mask:0xf bank_mask:0xf bound_ctrl:1
	v_pk_fma_f32 v[188:189], v[74:75], v[164:165], v[188:189] op_sel_hi:[1,0,1]
	v_pk_fma_f32 v[190:191], v[76:77], v[164:165], v[190:191] op_sel:[0,1,0] op_sel_hi:[1,1,1]
	v_pk_fma_f32 v[70:71], v[252:253], v[170:171], v[184:185] op_sel_hi:[1,0,1]
	v_pk_fma_f32 v[72:73], v[252:253], v[170:171], v[186:187] op_sel:[0,1,0] op_sel_hi:[1,1,1]
	v_pk_fma_f32 v[74:75], v[252:253], v[172:173], v[188:189] op_sel_hi:[1,0,1]
	v_pk_fma_f32 v[76:77], v[252:253], v[172:173], v[190:191] op_sel:[0,1,0] op_sel_hi:[1,1,1]
	v_pk_mul_f32 v[194:195], v[70:71], v[178:179] op_sel_hi:[1,0]
	v_pk_fma_f32 v[194:195], v[72:73], v[178:179], v[194:195] op_sel:[0,1,0] op_sel_hi:[1,1,1]
	v_pk_fma_f32 v[194:195], v[74:75], v[180:181], v[194:195] op_sel_hi:[1,0,1]
	v_pk_fma_f32 v[194:195], v[76:77], v[180:181], v[194:195] op_sel:[0,1,0] op_sel_hi:[1,1,1]

	s_waitcnt lgkmcnt(0)
	ds_read_b128 v[162:165], v79 offset:0x1f00
	ds_read_b128 v[166:169], v79 offset:0x3f00
	ds_read_b128 v[170:173], v79 offset:0x5f00
	ds_read_b128 v[174:177], v79 offset:0x7f00
	ds_read_b128 v[178:181], v79 offset:0x9f00
	ds_read_b32 v182, v80 offset:0xf80
	ds_read_b32 v183, v81 offset:0xf80
	v_pk_mul_f32 v[250:251], v[70:71], v[86:87] op_sel_hi:[1,0]
	v_pk_fma_f32 v[250:251], v[72:73], v[86:87], v[250:251] op_sel:[0,1,0] op_sel_hi:[1,1,1]
	v_pk_fma_f32 v[250:251], v[74:75], v[88:89], v[250:251] op_sel_hi:[1,0,1]
	v_pk_fma_f32 v[250:251], v[76:77], v[88:89], v[250:251] op_sel:[0,1,0] op_sel_hi:[1,1,1]
	v_pk_mul_f32 v[184:185], v[126:127], v[118:119] op_sel_hi:[1,0]
	v_pk_mul_f32 v[186:187], v[126:127], v[118:119] op_sel:[0,1] op_sel_hi:[1,1]
	v_add_f32_dpp v252, v251, v250 quad_perm:[1,0,3,2] row_mask:0xf bank_mask:0xf bound_ctrl:1
	v_add_f32_dpp v161, v195, v194 quad_perm:[1,0,3,2] row_mask:0xf bank_mask:0xf bound_ctrl:1
	v_pk_mul_f32 v[188:189], v[126:127], v[120:121] op_sel_hi:[1,0]
	v_add_f32_dpp v252, v252, v252 quad_perm:[2,3,0,1] row_mask:0xf bank_mask:0xf bound_ctrl:1
	v_add_f32_dpp v161, v161, v161 quad_perm:[2,3,0,1] row_mask:0xf bank_mask:0xf bound_ctrl:1
	v_pk_mul_f32 v[190:191], v[126:127], v[120:121] op_sel:[0,1] op_sel_hi:[1,1]
	v_add_f32_dpp v252, v252, v252 row_ror:4 row_mask:0xf bank_mask:0xf bound_ctrl:1
	v_add_f32_dpp v161, v161, v161 row_ror:4 row_mask:0xf bank_mask:0xf bound_ctrl:1
	v_pk_fma_f32 v[184:185], v[70:71], v[82:83], v[184:185] op_sel_hi:[1,0,1]
	v_add_f32_dpp v252, v252, v252 row_ror:8 row_mask:0xf bank_mask:0xf bound_ctrl:1
	v_add_f32_dpp v92, v161, v161 row_ror:8 row_mask:0xf bank_mask:0x2 bound_ctrl:1
	v_pk_fma_f32 v[186:187], v[72:73], v[82:83], v[186:187] op_sel:[0,1,0] op_sel_hi:[1,1,1]
	v_mov_b32_dpp v253, v252 quad_perm:[1,0,3,2] row_mask:0xf bank_mask:0xf bound_ctrl:1
	v_pk_fma_f32 v[188:189], v[74:75], v[84:85], v[188:189] op_sel_hi:[1,0,1]
	v_pk_fma_f32 v[190:191], v[76:77], v[84:85], v[190:191] op_sel:[0,1,0] op_sel_hi:[1,1,1]
	v_pk_fma_f32 v[70:71], v[252:253], v[114:115], v[184:185] op_sel_hi:[1,0,1]
	v_pk_fma_f32 v[72:73], v[252:253], v[114:115], v[186:187] op_sel:[0,1,0] op_sel_hi:[1,1,1]
	v_pk_fma_f32 v[74:75], v[252:253], v[116:117], v[188:189] op_sel_hi:[1,0,1]
	v_pk_fma_f32 v[76:77], v[252:253], v[116:117], v[190:191] op_sel:[0,1,0] op_sel_hi:[1,1,1]
	v_pk_mul_f32 v[192:193], v[70:71], v[122:123] op_sel_hi:[1,0]
	v_pk_fma_f32 v[192:193], v[72:73], v[122:123], v[192:193] op_sel:[0,1,0] op_sel_hi:[1,1,1]
	v_pk_fma_f32 v[192:193], v[74:75], v[124:125], v[192:193] op_sel_hi:[1,0,1]
	v_pk_fma_f32 v[192:193], v[76:77], v[124:125], v[192:193] op_sel:[0,1,0] op_sel_hi:[1,1,1]

	s_waitcnt lgkmcnt(0)
	ds_read_b128 v[82:85], v79 offset:0x2000
	ds_read_b128 v[86:89], v79 offset:0x4000
	ds_read_b128 v[114:117], v79 offset:0x6000
	ds_read_b128 v[118:121], v79 offset:0x8000
	ds_read_b128 v[122:125], v79 offset:0xa000
	ds_read_b32 v79, v80 offset:0x1000
	ds_read_b32 v161, v81 offset:0x1000
	v_pk_mul_f32 v[250:251], v[70:71], v[166:167] op_sel_hi:[1,0]
	v_pk_fma_f32 v[250:251], v[72:73], v[166:167], v[250:251] op_sel:[0,1,0] op_sel_hi:[1,1,1]
	v_pk_fma_f32 v[250:251], v[74:75], v[168:169], v[250:251] op_sel_hi:[1,0,1]
	v_pk_fma_f32 v[250:251], v[76:77], v[168:169], v[250:251] op_sel:[0,1,0] op_sel_hi:[1,1,1]
	v_pk_mul_f32 v[80:81], v[182:183], v[174:175] op_sel_hi:[1,0]
	v_pk_mul_f32 v[126:127], v[182:183], v[174:175] op_sel:[0,1] op_sel_hi:[1,1]
	v_add_f32_dpp v252, v251, v250 quad_perm:[1,0,3,2] row_mask:0xf bank_mask:0xf bound_ctrl:1
	v_add_f32_dpp v190, v193, v192 quad_perm:[1,0,3,2] row_mask:0xf bank_mask:0xf bound_ctrl:1
	v_pk_mul_f32 v[184:185], v[182:183], v[176:177] op_sel_hi:[1,0]
	v_add_f32_dpp v252, v252, v252 quad_perm:[2,3,0,1] row_mask:0xf bank_mask:0xf bound_ctrl:1
	v_add_f32_dpp v190, v190, v190 quad_perm:[2,3,0,1] row_mask:0xf bank_mask:0xf bound_ctrl:1
	v_pk_mul_f32 v[186:187], v[182:183], v[176:177] op_sel:[0,1] op_sel_hi:[1,1]
	v_add_f32_dpp v252, v252, v252 row_ror:4 row_mask:0xf bank_mask:0xf bound_ctrl:1
	v_add_f32_dpp v190, v190, v190 row_ror:4 row_mask:0xf bank_mask:0xf bound_ctrl:1
	v_pk_fma_f32 v[80:81], v[70:71], v[162:163], v[80:81] op_sel_hi:[1,0,1]
	v_add_f32_dpp v252, v252, v252 row_ror:8 row_mask:0xf bank_mask:0xf bound_ctrl:1
	v_add_f32_dpp v92, v190, v190 row_ror:8 row_mask:0xf bank_mask:0x4 bound_ctrl:1
	v_pk_fma_f32 v[126:127], v[72:73], v[162:163], v[126:127] op_sel:[0,1,0] op_sel_hi:[1,1,1]
	v_mov_b32_dpp v253, v252 quad_perm:[1,0,3,2] row_mask:0xf bank_mask:0xf bound_ctrl:1
	v_pk_fma_f32 v[184:185], v[74:75], v[164:165], v[184:185] op_sel_hi:[1,0,1]
	v_pk_fma_f32 v[186:187], v[76:77], v[164:165], v[186:187] op_sel:[0,1,0] op_sel_hi:[1,1,1]
	v_pk_fma_f32 v[70:71], v[252:253], v[170:171], v[80:81] op_sel_hi:[1,0,1]
	v_pk_fma_f32 v[72:73], v[252:253], v[170:171], v[126:127] op_sel:[0,1,0] op_sel_hi:[1,1,1]
	v_pk_fma_f32 v[74:75], v[252:253], v[172:173], v[184:185] op_sel_hi:[1,0,1]
	v_pk_fma_f32 v[76:77], v[252:253], v[172:173], v[186:187] op_sel:[0,1,0] op_sel_hi:[1,1,1]
	v_pk_mul_f32 v[188:189], v[70:71], v[178:179] op_sel_hi:[1,0]
	v_pk_fma_f32 v[188:189], v[72:73], v[178:179], v[188:189] op_sel:[0,1,0] op_sel_hi:[1,1,1]
	v_pk_fma_f32 v[188:189], v[74:75], v[180:181], v[188:189] op_sel_hi:[1,0,1]
	v_pk_fma_f32 v[188:189], v[76:77], v[180:181], v[188:189] op_sel:[0,1,0] op_sel_hi:[1,1,1]

; __device__ __forceinline__ float pair16_sum(f32x2 p) { float x = p.x + dpp_mov<0xB1>(p.y); x = dpp_add<0x4E>(x); x = dpp_add<0x124>(x); x = dpp_add<0x128>(x); return x; }
; __device__ __forceinline__ void p4_scan(Frame& F) {
;     ...
;                     { const float y7 = pair16_sum(qq); ykeep = ((kap >> 1) == 7) ? y7 : ykeep; }
;                     yb[(24 + (kap >> 1)) * 32 + rown] = ykeep;
;                 }
;     ...
;                 asm volatile("s_waitcnt lgkmcnt(0)" ::: "memory"); __builtin_amdgcn_s_barrier(); asm volatile("" ::: "memory");
	s_waitcnt lgkmcnt(0)
	s_nop 0
	s_nop 0
	v_add_f32_dpp v79, v189, v188 quad_perm:[1,0,3,2] row_mask:0xf bank_mask:0xf bound_ctrl:1
	s_nop 1
	v_add_f32_dpp v79, v79, v79 quad_perm:[2,3,0,1] row_mask:0xf bank_mask:0xf bound_ctrl:1
	s_nop 1
	v_add_f32_dpp v79, v79, v79 row_ror:4 row_mask:0xf bank_mask:0xf bound_ctrl:1
	s_nop 1
	v_add_f32_dpp v92, v79, v79 row_ror:8 row_mask:0xf bank_mask:0x8 bound_ctrl:1
	ds_write_b32 v197, v92 offset:3584
	s_waitcnt lgkmcnt(0)
	s_barrier
	s_cbranch_scc1 .LBB0_489
	s_setprio 0
	s_mov_b64 s[2:3], 0
